# baseline (speedup 1.0000x reference)
_Z10ode_kernelPKfPKDF16_S2_PfPKi:
	v_lshrrev_b32_e32 v167, 6, v0
	s_lshr_b32 s3, s2, 3
	v_add_u32_e32 v2, s3, v167
	s_load_dwordx4 s[4:7], s[0:1], 0x0
	s_load_dwordx2 s[12:13], s[0:1], 0x10
	v_and_b32_e32 v130, 3, v2
	v_and_b32_e32 v1, 63, v0
	v_readfirstlane_b32 s3, v130
	v_lshlrev_b32_e32 v166, 4, v1
	s_lshl_b32 s11, s3, 14
	v_lshl_or_b32 v2, v130, 17, v166
	v_mov_b32_e32 v3, 0
	s_and_b32 s17, s11, 0xc000
	s_mov_b32 s9, 0
	s_waitcnt lgkmcnt(0)
	v_lshl_add_u64 v[74:75], s[6:7], 0, v[2:3]
	s_lshl_b32 s8, s17, 1
	v_lshl_add_u64 v[46:47], v[74:75], 0, s[8:9]
	s_movk_i32 s15, 0x1000
	v_add_co_u32_e32 v18, vcc, s15, v46
	s_movk_i32 s14, 0x3000
	s_nop 0
	v_addc_co_u32_e32 v19, vcc, 0, v47, vcc
	v_add_co_u32_e32 v20, vcc, s14, v46
	s_lshl_b32 s10, s2, 10
	s_nop 0
	v_addc_co_u32_e32 v21, vcc, 0, v47, vcc
	s_and_b32 s8, s10, 0x3e000
	s_movk_i32 s16, 0x7000
	v_add_co_u32_e32 v48, vcc, s16, v46
	v_lshl_or_b32 v22, v1, 7, s8
	s_add_i32 s8, s11, 0x4000
	v_addc_co_u32_e32 v49, vcc, 0, v47, vcc
	s_movk_i32 s16, 0x5000
	s_and_b32 s8, s8, 0xc000
	v_add_co_u32_e32 v50, vcc, s16, v46
	s_lshl_b32 s8, s8, 1
	global_load_dwordx4 v[34:37], v[18:19], off offset:2048
	global_load_dwordx4 v[14:17], v[20:21], off offset:2048
	global_load_dwordx4 v[6:9], v[20:21], off offset:1024
	global_load_dwordx4 v[2:5], v[18:19], off offset:1024
	global_load_dwordx4 v[42:45], v[18:19], off offset:3072
	global_load_dwordx4 v[38:41], v[20:21], off offset:3072
	v_addc_co_u32_e32 v51, vcc, 0, v47, vcc
	v_lshl_add_u64 v[72:73], v[74:75], 0, s[8:9]
	v_add_co_u32_e32 v106, vcc, s14, v72
	global_load_dwordx4 v[10:13], v[50:51], off offset:1024
	global_load_dwordx4 v[52:55], v[50:51], off offset:2048
	global_load_dwordx4 v[56:59], v[48:49], off offset:2048
	v_addc_co_u32_e32 v107, vcc, 0, v73, vcc
	v_add_co_u32_e32 v108, vcc, s15, v72
	global_load_dwordx4 v[60:63], v[50:51], off offset:3072
	global_load_dwordx4 v[64:67], v[48:49], off offset:3072
	global_load_ushort v198, v22, s[12:13]
	v_addc_co_u32_e32 v109, vcc, 0, v73, vcc
	global_load_dwordx4 v[68:71], v[108:109], off offset:2048
	global_load_dwordx4 v[78:81], v[106:107], off offset:2048
	global_load_dwordx4 v[82:85], v[106:107], off offset:3072
	global_load_dwordx4 v[86:89], v[108:109], off offset:3072
	s_add_i32 s8, s11, 0x6000
	s_movk_i32 s16, 0x2000
	s_and_b32 s8, s8, 0xe000
	v_add_co_u32_e32 v26, vcc, s16, v46
	s_lshl_b32 s8, s8, 1
	s_nop 0
	v_addc_co_u32_e32 v27, vcc, 0, v47, vcc
	v_lshl_add_u64 v[110:111], v[74:75], 0, s[8:9]
	v_add_co_u32_e32 v112, vcc, s14, v110
	global_load_dwordx4 a[0:3], v[46:47], off
	global_load_dwordx4 a[8:11], v[46:47], off offset:1024
	global_load_dwordx4 a[12:15], v[26:27], off offset:1024
	global_load_dwordx4 a[20:23], v[26:27], off offset:2048
	global_load_dwordx4 a[16:19], v[46:47], off offset:2048
	global_load_dwordx4 a[24:27], v[46:47], off offset:3072
	global_load_dwordx4 a[4:7], v[20:21], off offset:-4096
	global_load_dwordx4 v[22:25], v[20:21], off
	global_load_dwordx4 a[28:31], v[26:27], off offset:3072
	s_nop 0
	global_load_dwordx4 v[18:21], v[18:19], off
	v_addc_co_u32_e32 v113, vcc, 0, v111, vcc
	v_add_co_u32_e32 v114, vcc, s15, v110
	v_lshl_or_b32 v199, v167, 15, v166
	s_nop 0
	v_addc_co_u32_e32 v115, vcc, 0, v111, vcc
	global_load_dwordx4 v[26:29], v[114:115], off offset:1024
	global_load_dwordx4 v[90:93], v[114:115], off offset:2048
	global_load_dwordx4 v[30:33], v[112:113], off offset:1024
	global_load_dwordx4 v[94:97], v[112:113], off offset:2048
	global_load_dwordx4 v[98:101], v[114:115], off offset:3072
	global_load_dwordx4 v[102:105], v[112:113], off offset:3072
	s_movk_i32 s8, 0x6000
	s_load_dwordx2 s[6:7], s[0:1], 0x20
	v_lshlrev_b32_e32 v76, 1, v0
	v_and_b32_e32 v200, 7, v0
	v_and_b32_e32 v128, 64, v76
	v_and_b32_e32 v179, 15, v0
	v_bfe_u32 v201, v0, 4, 1
	v_mov_b32_e32 v196, 0x44444444
	global_load_dwordx4 a[44:47], v[48:49], off offset:-4096
	s_waitcnt vmcnt(31)
	ds_write_b128 v199, v[14:17] offset:1024
	v_add_co_u32_e32 v14, vcc, s8, v46
	s_movk_i32 s8, 0x4000
	s_nop 0
	v_addc_co_u32_e32 v15, vcc, 0, v47, vcc
	s_waitcnt vmcnt(28)
	ds_write_b128 v199, v[42:45] offset:2048
	v_add_co_u32_e32 v42, vcc, s8, v46
	ds_write_b128 v199, v[34:37]
	s_nop 0
	v_addc_co_u32_e32 v43, vcc, 0, v47, vcc
	s_waitcnt vmcnt(27)
	ds_write_b128 v199, v[38:41] offset:3072
	v_add_co_u32_e32 v44, vcc, s16, v72
	global_load_dwordx4 a[36:39], v[14:15], off offset:1024
	global_load_dwordx4 a[32:35], v[42:43], off offset:1024
	global_load_dwordx4 a[48:51], v[42:43], off offset:2048
	global_load_dwordx4 a[52:55], v[14:15], off offset:2048
	global_load_dwordx4 a[60:63], v[14:15], off offset:3072
	global_load_dwordx4 a[40:43], v[50:51], off offset:-4096
	global_load_dwordx4 v[34:37], v[50:51], off
	global_load_dwordx4 v[38:41], v[48:49], off
	s_nop 0
	global_load_dwordx4 v[14:17], v[48:49], off offset:1024
	s_waitcnt vmcnt(34)
	ds_write_b128 v199, v[52:55] offset:4096
	s_waitcnt vmcnt(33)
	ds_write_b128 v199, v[56:59] offset:5120
	v_addc_co_u32_e32 v45, vcc, 0, v73, vcc
	s_xor_b32 s8, s17, 0x8000
	global_load_dwordx4 a[68:71], v[106:107], off offset:-4096
	s_waitcnt vmcnt(33)
	ds_write_b128 v199, v[60:63] offset:6144
	s_waitcnt vmcnt(32)
	ds_write_b128 v199, v[64:67] offset:7168
	v_add_co_u32_e32 v58, vcc, s16, v110
	s_lshl_b32 s8, s8, 1
	global_load_dwordx4 a[56:59], v[42:43], off offset:3072
	global_load_dwordx4 a[64:67], v[72:73], off
	global_load_dwordx4 a[72:75], v[72:73], off offset:1024
	global_load_dwordx4 a[80:83], v[72:73], off offset:2048
	global_load_dwordx4 a[84:87], v[44:45], off offset:2048
	global_load_dwordx4 a[92:95], v[44:45], off offset:3072
	global_load_dwordx4 a[76:79], v[44:45], off offset:1024
	global_load_dwordx4 a[88:91], v[72:73], off offset:3072
	global_load_dwordx4 v[46:49], v[106:107], off
	global_load_dwordx4 v[54:57], v[106:107], off offset:1024
	s_nop 0
	global_load_dwordx4 v[42:45], v[108:109], off
	global_load_dwordx4 v[50:53], v[108:109], off offset:1024
	s_waitcnt vmcnt(42)
	ds_write_b128 v199, v[68:71] offset:8192
	s_waitcnt vmcnt(41)
	ds_write_b128 v199, v[78:81] offset:9216
	s_waitcnt vmcnt(39)
	ds_write_b128 v199, v[86:89] offset:10240
	ds_write_b128 v199, v[82:85] offset:11264
	v_addc_co_u32_e32 v59, vcc, 0, v111, vcc
	v_lshl_add_u64 v[78:79], v[74:75], 0, s[8:9]
	v_add_co_u32_e32 v84, vcc, s14, v78
	global_load_dwordx4 a[96:99], v[110:111], off
	global_load_dwordx4 a[104:107], v[110:111], off offset:1024
	global_load_dwordx4 a[108:111], v[58:59], off offset:1024
	global_load_dwordx4 a[116:119], v[58:59], off offset:2048
	global_load_dwordx4 a[112:115], v[110:111], off offset:2048
	global_load_dwordx4 a[120:123], v[110:111], off offset:3072
	global_load_dwordx4 a[100:103], v[112:113], off offset:-4096
	global_load_dwordx4 v[62:65], v[112:113], off
	global_load_dwordx4 a[124:127], v[58:59], off offset:3072
	s_nop 0
	global_load_dwordx4 v[58:61], v[114:115], off
	v_addc_co_u32_e32 v85, vcc, 0, v79, vcc
	v_add_co_u32_e32 v82, vcc, s15, v78
	s_add_i32 s8, s11, 0xa000
	s_nop 0
	v_addc_co_u32_e32 v83, vcc, 0, v79, vcc
	global_load_dwordx4 v[110:113], v[82:83], off offset:2048
	global_load_dwordx4 v[106:109], v[84:85], off offset:2048
	s_waitcnt vmcnt(39)
	ds_write_b128 v199, v[90:93] offset:12288
	s_waitcnt vmcnt(37)
	ds_write_b128 v199, v[94:97] offset:13312
	s_waitcnt vmcnt(36)
	ds_write_b128 v199, v[98:101] offset:14336
	s_waitcnt vmcnt(35)
	ds_write_b128 v199, v[102:105] offset:15360
	global_load_dwordx4 a[128:131], v[78:79], off
	global_load_dwordx4 a[132:135], v[84:85], off offset:-4096
	global_load_dwordx4 a[136:139], v[78:79], off offset:1024
	global_load_dwordx4 a[144:147], v[78:79], off offset:2048
	global_load_dwordx4 v[102:105], v[82:83], off offset:3072
	global_load_dwordx4 v[98:101], v[84:85], off offset:3072
	s_and_b32 s8, s8, 0xe000
	v_add_co_u32_e32 v80, vcc, s16, v78
	s_lshl_b32 s8, s8, 1
	s_nop 0
	v_addc_co_u32_e32 v81, vcc, 0, v79, vcc
	v_lshl_add_u64 v[122:123], v[74:75], 0, s[8:9]
	v_add_co_u32_e32 v124, vcc, s14, v122
	s_add_i32 s8, s11, 0xc000
	s_nop 0
	v_addc_co_u32_e32 v125, vcc, 0, v123, vcc
	v_add_co_u32_e32 v126, vcc, s15, v122
	s_and_b32 s8, s8, 0xc000
	s_nop 0
	v_addc_co_u32_e32 v127, vcc, 0, v123, vcc
	global_load_dwordx4 v[70:73], v[124:125], off offset:1024
	global_load_dwordx4 v[114:117], v[124:125], off offset:2048
	global_load_dwordx4 v[66:69], v[126:127], off offset:1024
	global_load_dwordx4 v[118:121], v[126:127], off offset:2048
	global_load_dwordx4 a[148:151], v[80:81], off offset:2048
	global_load_dwordx4 a[156:159], v[80:81], off offset:3072
	global_load_dwordx4 v[132:135], v[126:127], off offset:3072
	global_load_dwordx4 v[136:139], v[124:125], off offset:3072
	global_load_dwordx4 a[140:143], v[80:81], off offset:1024
	global_load_dwordx4 a[152:155], v[78:79], off offset:3072
	s_nop 0
	global_load_dwordx4 v[78:81], v[84:85], off
	global_load_dwordx4 v[86:89], v[84:85], off offset:1024
	s_lshl_b32 s8, s8, 1
	v_lshl_add_u64 v[164:165], v[74:75], 0, s[8:9]
	v_add_co_u32_e32 v176, vcc, s14, v164
	s_add_i32 s11, s11, 0xe000
	s_nop 0
	v_addc_co_u32_e32 v177, vcc, 0, v165, vcc
	v_add_co_u32_e32 v184, vcc, s15, v164
	s_and_b32 s8, s11, 0xe000
	s_nop 0
	v_addc_co_u32_e32 v185, vcc, 0, v165, vcc
	global_load_dwordx4 v[140:143], v[184:185], off offset:2048
	global_load_dwordx4 v[144:147], v[176:177], off offset:2048
	global_load_dwordx4 v[148:151], v[176:177], off offset:3072
	global_load_dwordx4 v[152:155], v[184:185], off offset:3072
	s_lshl_b32 s8, s8, 1
	v_lshl_add_u64 v[186:187], v[74:75], 0, s[8:9]
	v_add_co_u32_e32 v188, vcc, s14, v186
	v_and_or_b32 v74, v76, 16, v200
	s_nop 0
	v_addc_co_u32_e32 v189, vcc, 0, v187, vcc
	v_add_co_u32_e32 v190, vcc, s15, v186
	v_lshlrev_b32_e32 v129, 2, v74
	s_nop 0
	v_addc_co_u32_e32 v191, vcc, 0, v187, vcc
	global_load_dwordx4 v[94:97], v[188:189], off offset:1024
	global_load_dwordx4 v[156:159], v[188:189], off offset:2048
	global_load_dwordx4 v[90:93], v[190:191], off offset:1024
	global_load_dwordx4 v[160:163], v[190:191], off offset:2048
	global_load_dwordx4 v[172:175], v[188:189], off offset:3072
	global_load_dwordx4 v[180:183], v[190:191], off offset:3072
	s_waitcnt lgkmcnt(0)
	global_load_dword v131, v129, s[6:7]
	global_load_dwordx4 v[74:77], v[82:83], off
	s_nop 0
	global_load_dwordx4 v[82:85], v[82:83], off offset:1024
	s_waitcnt vmcnt(32)
	ds_write_b128 v199, v[110:113] offset:16384
	s_waitcnt vmcnt(31)
	ds_write_b128 v199, v[106:109] offset:17408
	v_lshlrev_b32_e32 v106, 7, v130
	v_or3_b32 v202, v106, v128, v179
	v_lshlrev_b32_e32 v106, 9, v201
	v_or_b32_e32 v107, 32, v129
	v_or3_b32 v106, v106, s10, v202
	global_load_dword v178, v129, s[6:7] offset:128
	global_load_dword v192, v107, s[6:7] offset:128
	global_load_dword v193, v129, s[6:7] offset:32
	v_ashrrev_i32_e32 v107, 31, v106
	v_lshl_add_u64 v[128:129], v[106:107], 2, s[4:5]
	global_load_dword v171, v[128:129], off
	s_waitcnt vmcnt(30)
	ds_write_b128 v199, v[102:105] offset:18432
	s_waitcnt vmcnt(29)
	ds_write_b128 v199, v[98:101] offset:19456
	v_add_co_u32_e32 v98, vcc, s16, v122
	s_mov_b32 s14, 0x45000000
	s_nop 0
	v_addc_co_u32_e32 v99, vcc, 0, v123, vcc
	global_load_dwordx4 a[160:163], v[122:123], off
	global_load_dwordx4 a[168:171], v[122:123], off offset:1024
	global_load_dwordx4 a[172:175], v[98:99], off offset:1024
	global_load_dwordx4 a[180:183], v[98:99], off offset:2048
	global_load_dwordx4 a[176:179], v[122:123], off offset:2048
	global_load_dwordx4 a[184:187], v[122:123], off offset:3072
	global_load_dword v170, v[128:129], off offset:64
	global_load_dwordx4 a[164:167], v[124:125], off offset:-4096
	global_load_dwordx4 v[102:105], v[124:125], off
	global_load_dwordx4 a[188:191], v[98:99], off offset:3072
	s_nop 0
	global_load_dwordx4 v[98:101], v[126:127], off
	s_waitcnt vmcnt(36)
	ds_write_b128 v199, v[118:121] offset:20480
	ds_write_b128 v199, v[114:117] offset:21504
	global_load_dword v169, v[128:129], off offset:128
	v_add_co_u32_e32 v106, vcc, s16, v164
	s_waitcnt vmcnt(34)
	ds_write_b128 v199, v[132:135] offset:22528
	s_waitcnt vmcnt(33)
	ds_write_b128 v199, v[136:139] offset:23552
	v_addc_co_u32_e32 v107, vcc, 0, v165, vcc
	global_load_dwordx4 a[192:195], v[164:165], off
	global_load_dwordx4 a[196:199], v[176:177], off offset:-4096
	global_load_dwordx4 a[200:203], v[164:165], off offset:1024
	global_load_dwordx4 a[208:211], v[164:165], off offset:2048
	global_load_dwordx4 a[212:215], v[106:107], off offset:2048
	global_load_dwordx4 a[220:223], v[106:107], off offset:3072
	global_load_dwordx4 a[204:207], v[106:107], off offset:1024
	global_load_dwordx4 a[216:219], v[164:165], off offset:3072
	global_load_dwordx4 v[110:113], v[176:177], off
	global_load_dwordx4 v[118:121], v[176:177], off offset:1024
	s_nop 0
	global_load_dwordx4 v[106:109], v[184:185], off
	global_load_dwordx4 v[114:117], v[184:185], off offset:1024
	global_load_dword v168, v[128:129], off offset:192
	v_add_co_u32_e32 v122, vcc, s16, v186
	v_and_b32_e32 v133, 32, v0
	s_nop 0
	v_addc_co_u32_e32 v123, vcc, 0, v187, vcc
	s_waitcnt vmcnt(41)
	ds_write_b128 v199, v[140:143] offset:24576
	s_waitcnt vmcnt(40)
	ds_write_b128 v199, v[144:147] offset:25600
	s_waitcnt vmcnt(38)
	ds_write_b128 v199, v[152:155] offset:26624
	ds_write_b128 v199, v[148:151] offset:27648
	global_load_dwordx4 a[224:227], v[186:187], off
	global_load_dwordx4 a[232:235], v[186:187], off offset:1024
	global_load_dwordx4 a[236:239], v[122:123], off offset:1024
	global_load_dwordx4 a[244:247], v[122:123], off offset:2048
	global_load_dwordx4 a[240:243], v[186:187], off offset:2048
	global_load_dwordx4 a[248:251], v[186:187], off offset:3072
	global_load_dwordx4 a[228:231], v[188:189], off offset:-4096
	global_load_dwordx4 v[126:129], v[188:189], off
	global_load_dwordx4 a[252:255], v[122:123], off offset:3072
	s_nop 0
	global_load_dwordx4 v[122:125], v[190:191], off
	v_lshlrev_b32_e32 v132, 2, v201
	v_lshl_or_b32 v130, v130, 6, v133
	v_lshrrev_b32_e32 v139, 1, v0
	v_and_b32_e32 v203, 24, v139
	s_waitcnt vmcnt(44)
	ds_write_b128 v199, v[160:163] offset:28672
	ds_write_b128 v199, v[156:159] offset:29696
	s_waitcnt vmcnt(42)
	ds_write_b128 v199, v[180:183] offset:30720
	ds_write_b128 v199, v[172:175] offset:31744
	s_waitcnt vmcnt(10) lgkmcnt(0)
	v_lshrrev_b32_e32 v222, 2, v131
	v_and_or_b32 v222, v222, 8, v132
	v_mul_u32_u24_e32 v222, 0x110, v222
	v_and_or_b32 v223, v131, 31, v130
	v_add_lshl_u32 v223, v223, v222, 1
	v_or_b32_e32 v204, 0x20000, v223
	v_lshrrev_b32_e32 v222, 2, v178
	v_and_or_b32 v222, v222, 8, v132
	v_mul_u32_u24_e32 v222, 0x110, v222
	v_and_or_b32 v223, v178, 31, v130
	v_add_lshl_u32 v223, v223, v222, 1
	v_or_b32_e32 v205, 0x20000, v223
	v_lshrrev_b32_e32 v222, 2, v193
	v_and_or_b32 v222, v222, 8, v132
	v_mul_u32_u24_e32 v222, 0x110, v222
	v_and_or_b32 v223, v193, 31, v130
	v_add_lshl_u32 v223, v223, v222, 1
	v_or_b32_e32 v206, 0x20000, v223
	v_lshrrev_b32_e32 v222, 2, v192
	v_and_or_b32 v222, v222, 8, v132
	v_mul_u32_u24_e32 v222, 0x110, v222
	v_and_or_b32 v223, v192, 31, v130
	v_add_lshl_u32 v223, v223, v222, 1
	v_or_b32_e32 v207, 0x20000, v223
	s_movk_i32 s43, 0x110
	v_mad_u32_u24 v224, v179, s43, v203
	v_mov_b32_e32 v225, 0x20000
	v_lshl_or_b32 v224, v224, 1, v225
	s_lshl_b32 s43, s3, 1
	s_add_u32 s52, s43, 0
	s_and_b32 s52, s52, 7
	s_lshl_b32 s52, s52, 6
	s_nop 0
	v_add_u32_e32 v208, s52, v224
	s_add_u32 s52, s43, 1
	s_and_b32 s52, s52, 7
	s_lshl_b32 s52, s52, 6
	s_sub_u32 s52, s52, 64
	s_nop 0
	v_add_u32_e32 v209, s52, v224
	s_add_u32 s52, s43, 2
	s_and_b32 s52, s52, 7
	s_lshl_b32 s52, s52, 6
	s_nop 0
	v_add_u32_e32 v211, s52, v224
	s_add_u32 s52, s43, 3
	s_and_b32 s52, s52, 7
	s_lshl_b32 s52, s52, 6
	s_nop 0
	v_add_u32_e32 v212, s52, v224
	s_add_u32 s52, s43, 4
	s_and_b32 s52, s52, 7
	s_lshl_b32 s52, s52, 6
	s_nop 0
	v_add_u32_e32 v213, s52, v224
	s_add_u32 s52, s43, 5
	s_and_b32 s52, s52, 7
	s_lshl_b32 s52, s52, 6
	s_nop 0
	v_add_u32_e32 v214, s52, v224
	s_add_u32 s52, s43, 6
	s_and_b32 s52, s52, 7
	s_lshl_b32 s52, s52, 6
	s_nop 0
	v_add_u32_e32 v215, s52, v224
	s_add_u32 s52, s43, 7
	s_and_b32 s52, s52, 7
	s_lshl_b32 s52, s52, 6
	s_nop 0
	v_add_u32_e32 v216, s52, v224
	v_and_b32_e32 v225, 8, v0
	v_cmp_eq_u32_e32 vcc, 0, v225
	v_mov_b32_e32 v225, 0xeeeeeeee
	s_nop 1
	v_cndmask_b32_e32 v210, v225, v196, vcc
	v_and_b32_e32 v225, 47, v0
	v_cmp_eq_u32_e64 s[4:5], 0, v225
	v_lshlrev_b32_e32 v225, 4, v167
	v_lshlrev_b32_e32 v226, 3, v201
	s_mov_b32 s52, 0x24400
	v_or3_b32 v218, v225, v226, s52
	s_load_dwordx2 s[6:7], s[0:1], 0x18
	s_lshl_b32 s11, s2, 9
	s_mov_b64 s[22:23], 0
	s_mov_b32 s29, 0
	s_mov_b32 s30, 0
	v_mov_b32_e32 v221, 0
	s_mov_b32 s40, 0x3a000000
	s_mov_b32 s41, 0x34800000
	s_mov_b32 s42, 0x45000000
	v_mov_b32_e32 v217, 0x24480
	v_mov_b64_e32 v[230:231], 0
	v_mov_b64_e32 v[232:233], 0
	v_mov_b64_e32 v[234:235], 0
	v_mov_b64_e32 v[236:237], 0
	v_mov_b64_e32 v[238:239], 0
	v_mov_b64_e32 v[240:241], 0
	v_mov_b64_e32 v[242:243], 0
	v_mov_b64_e32 v[244:245], 0
	ds_write_b128 v217, v[230:233]
	v_mov_b32_e32 v178, 0
	v_fma_mixlo_f16 v131, v178, v238, v171
	v_fma_mixlo_f16 v139, v178, v238, v170
	v_fma_mixlo_f16 v147, v178, v238, v169
	v_fma_mixlo_f16 v155, v178, v238, v168
	v_fma_f32 v130, v178, v238, v171
	v_fma_f32 v138, v178, v238, v170
	v_fma_f32 v146, v178, v238, v169
	v_fma_f32 v154, v178, v238, v168
	v_fma_mix_f32 v130, v130, 1.0, -v131 op_sel_hi:[0,0,1]
	v_fma_mix_f32 v138, v138, 1.0, -v139 op_sel_hi:[0,0,1]
	v_fma_mix_f32 v146, v146, 1.0, -v147 op_sel_hi:[0,0,1]
	v_fma_mix_f32 v154, v154, 1.0, -v155 op_sel_hi:[0,0,1]
	v_fma_mixlo_f16 v133, v130, s42, 0
	v_fma_mixlo_f16 v141, v138, s42, 0
	v_fma_mixlo_f16 v149, v146, s42, 0
	v_fma_mixlo_f16 v157, v154, s42, 0
	v_fma_mix_f32 v130, v130, s42, -v133 op_sel_hi:[0,0,1]
	v_fma_mix_f32 v138, v138, s42, -v141 op_sel_hi:[0,0,1]
	v_fma_mix_f32 v146, v146, s42, -v149 op_sel_hi:[0,0,1]
	v_fma_mix_f32 v154, v154, s42, -v157 op_sel_hi:[0,0,1]
	v_fma_mixlo_f16 v132, v130, s42, 0
	v_fma_mixlo_f16 v140, v138, s42, 0
	v_fma_mixlo_f16 v148, v146, s42, 0
	v_fma_mixlo_f16 v156, v154, s42, 0
	ds_write_b16 v204, v131
	ds_write_b16 v205, v139
	ds_write_b16 v206, v147
	ds_write_b16 v207, v155
	ds_write_b16 v204, v133 offset:544
	ds_write_b16 v205, v141 offset:544
	ds_write_b16 v206, v149 offset:544
	ds_write_b16 v207, v157 offset:544
	ds_write_b16 v204, v132 offset:1088
	ds_write_b16 v205, v140 offset:1088
	ds_write_b16 v206, v148 offset:1088
	ds_write_b16 v207, v156 offset:1088
	ds_read_b128 v[180:183], v199 offset:0
	s_waitcnt lgkmcnt(6)
	ds_read_b128 v[184:187], v199 offset:1024
	ds_read_b128 v[188:191], v199 offset:4096
	ds_read_b128 v[192:195], v199 offset:5120
	ds_read_b128 v[222:225], v199 offset:8192
	ds_read_b128 v[226:229], v199 offset:9216
	s_mov_b32 s52, 0x3a83126f
	v_mov_b32_e32 v248, 0x358637bd
	s_waitcnt lgkmcnt(0)
	s_barrier
	ds_read_b128 v[130:133], v208
	ds_read_b128 v[134:137], v209 offset:64
	ds_read_b128 v[138:141], v211
	ds_read_b128 v[142:145], v212
	ds_read_b128 v[146:149], v213
	ds_read_b128 v[150:153], v214
	ds_read_b128 v[154:157], v215
	ds_read_b128 v[158:161], v216
	s_waitcnt lgkmcnt(7)
	v_smfmac_f32_16x16x64_f16 v[230:233], v[130:133], a[16:23], v210
	v_fma_f32 v179, |v171|, s52, v248
	v_fma_f32 v196, |v170|, s52, v248
	v_smfmac_f32_16x16x64_f16 v[234:237], v[130:133], v[180:187], v210
	ds_read_b128 v[180:183], v199 offset:12288
	ds_read_b128 v[184:187], v199 offset:13312
	s_waitcnt lgkmcnt(8)
	v_smfmac_f32_16x16x64_f16 v[230:233], v[134:137], a[48:55], v210
	v_fma_f32 v197, |v169|, s52, v248
	v_fma_f32 v198, |v168|, s52, v248
	v_smfmac_f32_16x16x64_f16 v[234:237], v[134:137], v[188:195], v210
	ds_read_b128 v[188:191], v199 offset:16384
	ds_read_b128 v[192:195], v199 offset:17408
	s_waitcnt lgkmcnt(9)
	v_smfmac_f32_16x16x64_f16 v[230:233], v[138:141], a[80:87], v210
	v_rcp_f32_e32 v179, v179
	v_rcp_f32_e32 v196, v196
	v_smfmac_f32_16x16x64_f16 v[234:237], v[138:141], v[222:229], v210
	ds_read_b128 v[222:225], v199 offset:20480
	ds_read_b128 v[226:229], v199 offset:21504
	s_waitcnt lgkmcnt(10)
	v_smfmac_f32_16x16x64_f16 v[230:233], v[142:145], a[112:119], v210
	v_rcp_f32_e32 v197, v197
	v_rcp_f32_e32 v198, v198
	s_waitcnt lgkmcnt(4)
	v_smfmac_f32_16x16x64_f16 v[234:237], v[142:145], v[180:187], v210
	ds_read_b128 v[180:183], v199 offset:24576
	ds_read_b128 v[184:187], v199 offset:25600
	v_smfmac_f32_16x16x64_f16 v[230:233], v[146:149], a[144:151], v210
	v_mul_f32_e32 v249, v170, v196
	v_mul_f32_e32 v166, v249, v249
	s_waitcnt lgkmcnt(4)
	v_smfmac_f32_16x16x64_f16 v[234:237], v[146:149], v[188:195], v210
	ds_read_b128 v[188:191], v199 offset:28672
	ds_read_b128 v[192:195], v199 offset:29696
	v_smfmac_f32_16x16x64_f16 v[230:233], v[150:153], a[176:183], v210
	v_mul_f32_e32 v249, v171, v179
	v_fmac_f32_e32 v166, v249, v249
	s_waitcnt lgkmcnt(4)
	v_smfmac_f32_16x16x64_f16 v[234:237], v[150:153], v[222:229], v210
	ds_read_b128 v[222:225], v199 offset:2048
	ds_read_b128 v[226:229], v199 offset:3072
	v_smfmac_f32_16x16x64_f16 v[230:233], v[154:157], a[208:215], v210
	v_mul_f32_e32 v249, v169, v197
	v_fmac_f32_e32 v166, v249, v249
	s_waitcnt lgkmcnt(4)
	v_smfmac_f32_16x16x64_f16 v[234:237], v[154:157], v[180:187], v210
	ds_read_b128 v[180:183], v199 offset:6144
	ds_read_b128 v[184:187], v199 offset:7168
	s_waitcnt vmcnt(0)
	v_smfmac_f32_16x16x64_f16 v[230:233], v[158:161], a[240:247], v210
	v_mul_f32_e32 v249, v168, v198
	v_fmac_f32_e32 v166, v249, v249
	s_waitcnt lgkmcnt(4)
	v_smfmac_f32_16x16x64_f16 v[234:237], v[158:161], v[188:195], v210
	ds_read_b128 v[188:191], v199 offset:10240
	ds_read_b128 v[192:195], v199 offset:11264
	v_smfmac_f32_16x16x64_f16 v[238:241], v[130:133], a[24:31], v210
	s_waitcnt lgkmcnt(4)
	v_smfmac_f32_16x16x64_f16 v[242:245], v[130:133], v[222:229], v210
	ds_read_b128 v[222:225], v199 offset:14336
	ds_read_b128 v[226:229], v199 offset:15360
	v_smfmac_f32_16x16x64_f16 v[238:241], v[134:137], a[56:63], v210
	v_fmac_f32_e32 v230, s40, v231
	v_fmac_f32_e32 v234, s40, v235
	s_waitcnt lgkmcnt(4)
	v_smfmac_f32_16x16x64_f16 v[242:245], v[134:137], v[180:187], v210
	ds_read_b128 v[180:183], v199 offset:18432
	ds_read_b128 v[184:187], v199 offset:19456
	v_smfmac_f32_16x16x64_f16 v[238:241], v[138:141], a[88:95], v210
	v_fmac_f32_e32 v230, s41, v232
	v_fmac_f32_e32 v234, s41, v236
	s_waitcnt lgkmcnt(4)
	v_smfmac_f32_16x16x64_f16 v[242:245], v[138:141], v[188:195], v210
	ds_read_b128 v[188:191], v199 offset:22528
	ds_read_b128 v[192:195], v199 offset:23552
	v_smfmac_f32_16x16x64_f16 v[238:241], v[142:145], a[120:127], v210
	v_permlane32_swap_b32_e32 v230, v234
	v_add_f32_e32 v175, v230, v234
	s_waitcnt lgkmcnt(4)
	v_smfmac_f32_16x16x64_f16 v[242:245], v[142:145], v[222:229], v210
	ds_read_b128 v[222:225], v199 offset:26624
	ds_read_b128 v[226:229], v199 offset:27648
	v_smfmac_f32_16x16x64_f16 v[238:241], v[146:149], a[152:159], v210
	ds_read_b128 v[230:233], v217
	ds_read_b128 v[234:237], v217
	s_waitcnt lgkmcnt(6)
	v_smfmac_f32_16x16x64_f16 v[242:245], v[146:149], v[180:187], v210
	ds_read_b128 v[180:183], v199 offset:30720
	ds_read_b128 v[184:187], v199 offset:31744
	v_smfmac_f32_16x16x64_f16 v[238:241], v[150:153], a[184:191], v210
	s_waitcnt lgkmcnt(6)
	v_smfmac_f32_16x16x64_f16 v[242:245], v[150:153], v[188:195], v210
	v_smfmac_f32_16x16x64_f16 v[238:241], v[154:157], a[216:223], v210
	s_waitcnt lgkmcnt(4)
	v_smfmac_f32_16x16x64_f16 v[242:245], v[154:157], v[222:229], v210
	v_smfmac_f32_16x16x64_f16 v[238:241], v[158:161], a[248:255], v210
	s_waitcnt lgkmcnt(0)
	v_smfmac_f32_16x16x64_f16 v[242:245], v[158:161], v[180:187], v210
	v_smfmac_f32_16x16x64_f16 v[230:233], v[130:133], a[0:7], v210
	v_smfmac_f32_16x16x64_f16 v[234:237], v[130:133], v[18:25], v210
	v_smfmac_f32_16x16x64_f16 v[230:233], v[134:137], a[40:47], v210
	v_fmac_f32_e32 v238, s40, v239
	v_fmac_f32_e32 v242, s40, v243
	v_smfmac_f32_16x16x64_f16 v[234:237], v[134:137], v[34:41], v210
	v_smfmac_f32_16x16x64_f16 v[230:233], v[138:141], a[64:71], v210
	v_fmac_f32_e32 v238, s41, v240
	v_fmac_f32_e32 v242, s41, v244
	v_smfmac_f32_16x16x64_f16 v[234:237], v[138:141], v[42:49], v210
	v_smfmac_f32_16x16x64_f16 v[230:233], v[142:145], a[96:103], v210
	v_permlane32_swap_b32_e32 v238, v242
	v_add_f32_e32 v174, v238, v242
	v_smfmac_f32_16x16x64_f16 v[234:237], v[142:145], v[58:65], v210
	v_smfmac_f32_16x16x64_f16 v[230:233], v[146:149], a[128:135], v210
	ds_read_b128 v[238:241], v217
	ds_read_b128 v[242:245], v217
	v_smfmac_f32_16x16x64_f16 v[234:237], v[146:149], v[74:81], v210
	v_smfmac_f32_16x16x64_f16 v[230:233], v[150:153], a[160:167], v210
	v_smfmac_f32_16x16x64_f16 v[234:237], v[150:153], v[98:105], v210
	v_smfmac_f32_16x16x64_f16 v[230:233], v[154:157], a[192:199], v210
	v_smfmac_f32_16x16x64_f16 v[234:237], v[154:157], v[106:113], v210
	v_smfmac_f32_16x16x64_f16 v[230:233], v[158:161], a[224:231], v210
	v_smfmac_f32_16x16x64_f16 v[234:237], v[158:161], v[122:129], v210
	s_waitcnt lgkmcnt(1)
	v_smfmac_f32_16x16x64_f16 v[238:241], v[130:133], a[8:15], v210
	s_waitcnt lgkmcnt(0)
	v_smfmac_f32_16x16x64_f16 v[242:245], v[130:133], v[2:9], v210
	v_smfmac_f32_16x16x64_f16 v[238:241], v[134:137], a[32:39], v210
	v_fmac_f32_e32 v230, s40, v231
	v_fmac_f32_e32 v234, s40, v235
	v_smfmac_f32_16x16x64_f16 v[242:245], v[134:137], v[10:17], v210
	v_smfmac_f32_16x16x64_f16 v[238:241], v[138:141], a[72:79], v210
	v_fmac_f32_e32 v230, s41, v232
	v_fmac_f32_e32 v234, s41, v236
	v_smfmac_f32_16x16x64_f16 v[242:245], v[138:141], v[50:57], v210
	v_smfmac_f32_16x16x64_f16 v[238:241], v[142:145], a[104:111], v210
	v_permlane32_swap_b32_e32 v230, v234
	v_add_f32_e32 v173, v230, v234
	v_smfmac_f32_16x16x64_f16 v[242:245], v[142:145], v[26:33], v210
	v_smfmac_f32_16x16x64_f16 v[238:241], v[146:149], a[136:143], v210
	ds_read_b128 v[230:233], v217
	ds_read_b128 v[234:237], v217
	v_smfmac_f32_16x16x64_f16 v[242:245], v[146:149], v[82:89], v210
	v_smfmac_f32_16x16x64_f16 v[238:241], v[150:153], a[168:175], v210
	v_smfmac_f32_16x16x64_f16 v[242:245], v[150:153], v[66:73], v210
	v_smfmac_f32_16x16x64_f16 v[238:241], v[154:157], a[200:207], v210
	v_smfmac_f32_16x16x64_f16 v[242:245], v[154:157], v[114:121], v210
	v_smfmac_f32_16x16x64_f16 v[238:241], v[158:161], a[232:239], v210
	v_smfmac_f32_16x16x64_f16 v[242:245], v[158:161], v[90:97], v210
	s_nop 6
	v_fmac_f32_e32 v238, s40, v239
	v_fmac_f32_e32 v242, s40, v243
	v_fmac_f32_e32 v238, s41, v240
	v_fmac_f32_e32 v242, s41, v244
	s_nop 1
	v_permlane32_swap_b32_e32 v238, v242
	v_add_f32_e32 v172, v238, v242
	ds_read_b128 v[180:183], v199 offset:0
	ds_read_b128 v[184:187], v199 offset:1024
	ds_read_b128 v[188:191], v199 offset:4096
	ds_read_b128 v[192:195], v199 offset:5120
	ds_read_b128 v[222:225], v199 offset:8192
	ds_read_b128 v[226:229], v199 offset:9216
	v_mul_f32_e32 v239, 0x3b000000, v172
	v_mul_f32_e32 v239, v239, v196
	v_mul_f32_e32 v167, v239, v239
	v_mul_f32_e32 v239, 0x3b000000, v173
	v_mul_f32_e32 v239, v239, v179
	v_fmac_f32_e32 v167, v239, v239
	v_mul_f32_e32 v239, 0x3b000000, v175
	v_mul_f32_e32 v239, v239, v197
	v_fmac_f32_e32 v167, v239, v239
	v_mul_f32_e32 v239, 0x3b000000, v174
	v_mul_f32_e32 v239, v239, v198
	v_fmac_f32_e32 v167, v239, v239
	v_mov_b32_e32 v130, v166
	v_mov_b32_e32 v131, v167
	s_nop 0
	v_add_f32_dpp v130, v130, v130 quad_perm:[1,0,3,2] row_mask:0xf bank_mask:0xf bound_ctrl:1
	v_add_f32_dpp v131, v131, v131 quad_perm:[1,0,3,2] row_mask:0xf bank_mask:0xf bound_ctrl:1
	s_nop 0
	v_add_f32_dpp v130, v130, v130 quad_perm:[2,3,0,1] row_mask:0xf bank_mask:0xf bound_ctrl:1
	v_add_f32_dpp v131, v131, v131 quad_perm:[2,3,0,1] row_mask:0xf bank_mask:0xf bound_ctrl:1
	s_nop 0
	v_add_f32_dpp v130, v130, v130 row_half_mirror row_mask:0xf bank_mask:0xf bound_ctrl:1
	v_add_f32_dpp v131, v131, v131 row_half_mirror row_mask:0xf bank_mask:0xf bound_ctrl:1
	s_nop 0
	v_add_f32_dpp v130, v130, v130 row_mirror row_mask:0xf bank_mask:0xf bound_ctrl:1
	v_add_f32_dpp v131, v131, v131 row_mirror row_mask:0xf bank_mask:0xf bound_ctrl:1
	v_mov_b32_e32 v240, v130
	v_mov_b32_e32 v241, v131
	s_nop 0
	v_permlane32_swap_b32_e32 v130, v240
	v_permlane32_swap_b32_e32 v131, v241
	v_add_f32_e32 v130, v130, v240
	v_add_f32_e32 v131, v131, v241
	v_add_u32_e32 v242, 0, v218
	v_lshlrev_b32_e32 v243, 3, v201
	v_or_b32_e32 v243, 0x24400, v243
	s_and_saveexec_b64 s[2:3], s[4:5]
	ds_write_b64 v242, v[130:131]
	s_or_b64 exec, exec, s[2:3]
	s_waitcnt lgkmcnt(0)
	s_barrier
	ds_read_b64 v[134:135], v243 offset:0
	ds_read_b64 v[138:139], v243 offset:16
	ds_read_b64 v[142:143], v243 offset:32
	ds_read_b64 v[146:147], v243 offset:48
	s_waitcnt lgkmcnt(2)
	v_add_f32_e32 v238, v134, v138
	s_waitcnt lgkmcnt(1)
	v_add_f32_e32 v238, v238, v142
	s_waitcnt lgkmcnt(0)
	v_add_f32_e32 v238, v238, v146
	v_add_f32_e32 v239, v135, v139
	v_add_f32_e32 v239, v239, v143
	v_add_f32_e32 v239, v239, v147
	v_mul_f32_e32 v238, 0x3b000000, v238
	v_max_f32_e32 v238, 0xda24260, v238
	v_sqrt_f32_e32 v238, v238
	v_mul_f32_e32 v239, 0x3b000000, v239
	v_max_f32_e32 v239, 0xda24260, v239
	v_sqrt_f32_e32 v239, v239
	s_nop 0
	v_mov_b32_e32 v220, v239
	v_rcp_f32_e32 v240, v239
	v_min_f32_e32 v241, v238, v239
	v_mul_f32_e32 v238, 0x3c23d70a, v238
	v_mul_f32_e32 v238, v238, v240
	s_mov_b32 s52, 0x3727c5ac
	v_cmp_ngt_f32_e32 vcc, s52, v241
	v_mov_b32_e32 v240, 0x358637bd
	s_nop 1
	v_cndmask_b32_e32 v219, v240, v238, vcc
	v_mul_f32_e32 v178, 0x3b000000, v219
	v_fma_mixlo_f16 v131, v178, v173, v171
	v_fma_mixlo_f16 v139, v178, v172, v170
	v_fma_mixlo_f16 v147, v178, v175, v169
	v_fma_mixlo_f16 v155, v178, v174, v168
	v_fma_f32 v130, v178, v173, v171
	v_fma_f32 v138, v178, v172, v170
	v_fma_f32 v146, v178, v175, v169
	v_fma_f32 v154, v178, v174, v168
	v_fma_mix_f32 v130, v130, 1.0, -v131 op_sel_hi:[0,0,1]
	v_fma_mix_f32 v138, v138, 1.0, -v139 op_sel_hi:[0,0,1]
	v_fma_mix_f32 v146, v146, 1.0, -v147 op_sel_hi:[0,0,1]
	v_fma_mix_f32 v154, v154, 1.0, -v155 op_sel_hi:[0,0,1]
	v_fma_mixlo_f16 v133, v130, s42, 0
	v_fma_mixlo_f16 v141, v138, s42, 0
	v_fma_mixlo_f16 v149, v146, s42, 0
	v_fma_mixlo_f16 v157, v154, s42, 0
	v_fma_mix_f32 v130, v130, s42, -v133 op_sel_hi:[0,0,1]
	v_fma_mix_f32 v138, v138, s42, -v141 op_sel_hi:[0,0,1]
	v_fma_mix_f32 v146, v146, s42, -v149 op_sel_hi:[0,0,1]
	v_fma_mix_f32 v154, v154, s42, -v157 op_sel_hi:[0,0,1]
	v_fma_mixlo_f16 v132, v130, s42, 0
	v_fma_mixlo_f16 v140, v138, s42, 0
	v_fma_mixlo_f16 v148, v146, s42, 0
	v_fma_mixlo_f16 v156, v154, s42, 0
	ds_write_b16 v204, v131 offset:8704
	ds_write_b16 v205, v139 offset:8704
	ds_write_b16 v206, v147 offset:8704
	ds_write_b16 v207, v155 offset:8704
	ds_write_b16 v204, v133 offset:9248
	ds_write_b16 v205, v141 offset:9248
	ds_write_b16 v206, v149 offset:9248
	ds_write_b16 v207, v157 offset:9248
	ds_write_b16 v204, v132 offset:9792
	ds_write_b16 v205, v140 offset:9792
	ds_write_b16 v206, v148 offset:9792
	ds_write_b16 v207, v156 offset:9792
	s_waitcnt lgkmcnt(0)
	s_barrier
	ds_read_b128 v[130:133], v208 offset:8704
	ds_read_b128 v[134:137], v209 offset:8768
	ds_read_b128 v[138:141], v211 offset:8704
	ds_read_b128 v[142:145], v212 offset:8704
	ds_read_b128 v[146:149], v213 offset:8704
	ds_read_b128 v[150:153], v214 offset:8704
	ds_read_b128 v[154:157], v215 offset:8704
	ds_read_b128 v[158:161], v216 offset:8704
	s_waitcnt lgkmcnt(7)
	v_smfmac_f32_16x16x64_f16 v[230:233], v[130:133], a[16:23], v210
	ds_read_b128 v[238:241], v217
	ds_read_b128 v[242:245], v217
	v_smfmac_f32_16x16x64_f16 v[234:237], v[130:133], v[180:187], v210
	ds_read_b128 v[180:183], v199 offset:12288
	ds_read_b128 v[184:187], v199 offset:13312
	s_waitcnt lgkmcnt(10)
	v_smfmac_f32_16x16x64_f16 v[230:233], v[134:137], a[48:55], v210
	v_smfmac_f32_16x16x64_f16 v[234:237], v[134:137], v[188:195], v210
	ds_read_b128 v[188:191], v199 offset:16384
	ds_read_b128 v[192:195], v199 offset:17408
	s_waitcnt lgkmcnt(11)
	v_smfmac_f32_16x16x64_f16 v[230:233], v[138:141], a[80:87], v210
	v_smfmac_f32_16x16x64_f16 v[234:237], v[138:141], v[222:229], v210
	ds_read_b128 v[222:225], v199 offset:20480
	ds_read_b128 v[226:229], v199 offset:21504
	s_waitcnt lgkmcnt(12)
	v_smfmac_f32_16x16x64_f16 v[230:233], v[142:145], a[112:119], v210
	s_waitcnt lgkmcnt(4)
	v_smfmac_f32_16x16x64_f16 v[234:237], v[142:145], v[180:187], v210
	ds_read_b128 v[180:183], v199 offset:24576
	ds_read_b128 v[184:187], v199 offset:25600
	v_smfmac_f32_16x16x64_f16 v[230:233], v[146:149], a[144:151], v210
	s_waitcnt lgkmcnt(4)
	v_smfmac_f32_16x16x64_f16 v[234:237], v[146:149], v[188:195], v210
	ds_read_b128 v[188:191], v199 offset:28672
	ds_read_b128 v[192:195], v199 offset:29696
	v_smfmac_f32_16x16x64_f16 v[230:233], v[150:153], a[176:183], v210
	s_waitcnt lgkmcnt(4)
	v_smfmac_f32_16x16x64_f16 v[234:237], v[150:153], v[222:229], v210
	ds_read_b128 v[222:225], v199 offset:2048
	ds_read_b128 v[226:229], v199 offset:3072
	v_smfmac_f32_16x16x64_f16 v[230:233], v[154:157], a[208:215], v210
	s_waitcnt lgkmcnt(4)
	v_smfmac_f32_16x16x64_f16 v[234:237], v[154:157], v[180:187], v210
	ds_read_b128 v[180:183], v199 offset:6144
	ds_read_b128 v[184:187], v199 offset:7168
	v_smfmac_f32_16x16x64_f16 v[230:233], v[158:161], a[240:247], v210
	s_waitcnt lgkmcnt(4)
	v_smfmac_f32_16x16x64_f16 v[234:237], v[158:161], v[188:195], v210
	ds_read_b128 v[188:191], v199 offset:10240
	ds_read_b128 v[192:195], v199 offset:11264
	v_smfmac_f32_16x16x64_f16 v[238:241], v[130:133], a[24:31], v210
	s_waitcnt lgkmcnt(4)
	v_smfmac_f32_16x16x64_f16 v[242:245], v[130:133], v[222:229], v210
	ds_read_b128 v[222:225], v199 offset:14336
	ds_read_b128 v[226:229], v199 offset:15360
	v_smfmac_f32_16x16x64_f16 v[238:241], v[134:137], a[56:63], v210
	v_fmac_f32_e32 v230, s40, v231
	v_fmac_f32_e32 v234, s40, v235
	s_waitcnt lgkmcnt(4)
	v_smfmac_f32_16x16x64_f16 v[242:245], v[134:137], v[180:187], v210
	ds_read_b128 v[180:183], v199 offset:18432
	ds_read_b128 v[184:187], v199 offset:19456
	v_smfmac_f32_16x16x64_f16 v[238:241], v[138:141], a[88:95], v210
	v_fmac_f32_e32 v230, s41, v232
	v_fmac_f32_e32 v234, s41, v236
	s_waitcnt lgkmcnt(4)
	v_smfmac_f32_16x16x64_f16 v[242:245], v[138:141], v[188:195], v210
	ds_read_b128 v[188:191], v199 offset:22528
	ds_read_b128 v[192:195], v199 offset:23552
	v_smfmac_f32_16x16x64_f16 v[238:241], v[142:145], a[120:127], v210
	v_permlane32_swap_b32_e32 v230, v234
	v_add_f32_e32 v164, v230, v234
	s_waitcnt lgkmcnt(4)
	v_smfmac_f32_16x16x64_f16 v[242:245], v[142:145], v[222:229], v210
	ds_read_b128 v[222:225], v199 offset:26624
	ds_read_b128 v[226:229], v199 offset:27648
	v_smfmac_f32_16x16x64_f16 v[238:241], v[146:149], a[152:159], v210
	ds_read_b128 v[230:233], v217
	ds_read_b128 v[234:237], v217
	s_waitcnt lgkmcnt(6)
	v_smfmac_f32_16x16x64_f16 v[242:245], v[146:149], v[180:187], v210
	ds_read_b128 v[180:183], v199 offset:30720
	ds_read_b128 v[184:187], v199 offset:31744
	v_smfmac_f32_16x16x64_f16 v[238:241], v[150:153], a[184:191], v210
	s_waitcnt lgkmcnt(6)
	v_smfmac_f32_16x16x64_f16 v[242:245], v[150:153], v[188:195], v210
	v_smfmac_f32_16x16x64_f16 v[238:241], v[154:157], a[216:223], v210
	s_waitcnt lgkmcnt(4)
	v_smfmac_f32_16x16x64_f16 v[242:245], v[154:157], v[222:229], v210
	v_smfmac_f32_16x16x64_f16 v[238:241], v[158:161], a[248:255], v210
	s_waitcnt lgkmcnt(0)
	v_smfmac_f32_16x16x64_f16 v[242:245], v[158:161], v[180:187], v210
	v_smfmac_f32_16x16x64_f16 v[230:233], v[130:133], a[0:7], v210
	v_smfmac_f32_16x16x64_f16 v[234:237], v[130:133], v[18:25], v210
	v_smfmac_f32_16x16x64_f16 v[230:233], v[134:137], a[40:47], v210
	v_fmac_f32_e32 v238, s40, v239
	v_fmac_f32_e32 v242, s40, v243
	v_smfmac_f32_16x16x64_f16 v[234:237], v[134:137], v[34:41], v210
	v_smfmac_f32_16x16x64_f16 v[230:233], v[138:141], a[64:71], v210
	v_fmac_f32_e32 v238, s41, v240
	v_fmac_f32_e32 v242, s41, v244
	v_smfmac_f32_16x16x64_f16 v[234:237], v[138:141], v[42:49], v210
	v_smfmac_f32_16x16x64_f16 v[230:233], v[142:145], a[96:103], v210
	v_permlane32_swap_b32_e32 v238, v242
	v_add_f32_e32 v165, v238, v242
	v_smfmac_f32_16x16x64_f16 v[234:237], v[142:145], v[58:65], v210
	v_smfmac_f32_16x16x64_f16 v[230:233], v[146:149], a[128:135], v210
	ds_read_b128 v[238:241], v217
	ds_read_b128 v[242:245], v217
	v_smfmac_f32_16x16x64_f16 v[234:237], v[146:149], v[74:81], v210
	v_smfmac_f32_16x16x64_f16 v[230:233], v[150:153], a[160:167], v210
	v_smfmac_f32_16x16x64_f16 v[234:237], v[150:153], v[98:105], v210
	v_smfmac_f32_16x16x64_f16 v[230:233], v[154:157], a[192:199], v210
	v_smfmac_f32_16x16x64_f16 v[234:237], v[154:157], v[106:113], v210
	v_smfmac_f32_16x16x64_f16 v[230:233], v[158:161], a[224:231], v210
	v_smfmac_f32_16x16x64_f16 v[234:237], v[158:161], v[122:129], v210
	s_waitcnt lgkmcnt(1)
	v_smfmac_f32_16x16x64_f16 v[238:241], v[130:133], a[8:15], v210
	s_waitcnt lgkmcnt(0)
	v_smfmac_f32_16x16x64_f16 v[242:245], v[130:133], v[2:9], v210
	v_smfmac_f32_16x16x64_f16 v[238:241], v[134:137], a[32:39], v210
	v_fmac_f32_e32 v230, s40, v231
	v_fmac_f32_e32 v234, s40, v235
	v_smfmac_f32_16x16x64_f16 v[242:245], v[134:137], v[10:17], v210
	v_smfmac_f32_16x16x64_f16 v[238:241], v[138:141], a[72:79], v210
	v_fmac_f32_e32 v230, s41, v232
	v_fmac_f32_e32 v234, s41, v236
	v_smfmac_f32_16x16x64_f16 v[242:245], v[138:141], v[50:57], v210
	v_smfmac_f32_16x16x64_f16 v[238:241], v[142:145], a[104:111], v210
	v_permlane32_swap_b32_e32 v230, v234
	v_add_f32_e32 v162, v230, v234
	v_smfmac_f32_16x16x64_f16 v[242:245], v[142:145], v[26:33], v210
	v_smfmac_f32_16x16x64_f16 v[238:241], v[146:149], a[136:143], v210
	ds_read_b128 v[230:233], v217
	ds_read_b128 v[234:237], v217
	v_smfmac_f32_16x16x64_f16 v[242:245], v[146:149], v[82:89], v210
	v_smfmac_f32_16x16x64_f16 v[238:241], v[150:153], a[168:175], v210
	v_smfmac_f32_16x16x64_f16 v[242:245], v[150:153], v[66:73], v210
	v_smfmac_f32_16x16x64_f16 v[238:241], v[154:157], a[200:207], v210
	v_smfmac_f32_16x16x64_f16 v[242:245], v[154:157], v[114:121], v210
	v_smfmac_f32_16x16x64_f16 v[238:241], v[158:161], a[232:239], v210
	v_smfmac_f32_16x16x64_f16 v[242:245], v[158:161], v[90:97], v210
	s_nop 6
	v_fmac_f32_e32 v238, s40, v239
	v_fmac_f32_e32 v242, s40, v243
	v_fmac_f32_e32 v238, s41, v240
	v_fmac_f32_e32 v242, s41, v244
	s_nop 1
	v_permlane32_swap_b32_e32 v238, v242
	v_add_f32_e32 v163, v238, v242
	ds_read_b128 v[180:183], v199 offset:0
	ds_read_b128 v[184:187], v199 offset:1024
	ds_read_b128 v[188:191], v199 offset:4096
	ds_read_b128 v[192:195], v199 offset:5120
	ds_read_b128 v[222:225], v199 offset:8192
	ds_read_b128 v[226:229], v199 offset:9216
	v_sub_f32_e32 v238, v163, v172
	v_mul_f32_e32 v238, 0x3b000000, v238
	v_mul_f32_e32 v238, v238, v196
	v_mul_f32_e32 v130, v238, v238
	v_sub_f32_e32 v238, v162, v173
	v_mul_f32_e32 v238, 0x3b000000, v238
	v_mul_f32_e32 v238, v238, v179
	v_fmac_f32_e32 v130, v238, v238
	v_sub_f32_e32 v238, v164, v175
	v_mul_f32_e32 v238, 0x3b000000, v238
	v_mul_f32_e32 v238, v238, v197
	v_fmac_f32_e32 v130, v238, v238
	v_sub_f32_e32 v238, v165, v174
	v_mul_f32_e32 v238, 0x3b000000, v238
	v_mul_f32_e32 v238, v238, v198
	v_fmac_f32_e32 v130, v238, v238
	s_nop 1
	v_add_f32_dpp v130, v130, v130 quad_perm:[1,0,3,2] row_mask:0xf bank_mask:0xf bound_ctrl:1
	s_nop 1
	v_add_f32_dpp v130, v130, v130 quad_perm:[2,3,0,1] row_mask:0xf bank_mask:0xf bound_ctrl:1
	s_nop 1
	v_add_f32_dpp v130, v130, v130 row_half_mirror row_mask:0xf bank_mask:0xf bound_ctrl:1
	s_nop 1
	v_add_f32_dpp v130, v130, v130 row_mirror row_mask:0xf bank_mask:0xf bound_ctrl:1
	v_mov_b32_e32 v240, v130
	s_nop 1
	v_permlane32_swap_b32_e32 v130, v240
	v_add_f32_e32 v130, v130, v240
	v_add_u32_e32 v242, 64, v218
	v_lshlrev_b32_e32 v243, 3, v201
	v_or_b32_e32 v243, 0x24440, v243
	s_and_saveexec_b64 s[2:3], s[4:5]
	ds_write_b32 v242, v130
	s_or_b64 exec, exec, s[2:3]
	s_waitcnt lgkmcnt(0)
	s_barrier
	ds_read2_b32 v[134:135], v243 offset1:4
	ds_read2_b32 v[136:137], v243 offset0:8 offset1:12
	s_waitcnt lgkmcnt(1)
	v_add_f32_e32 v238, v134, v135
	s_waitcnt lgkmcnt(0)
	v_add_f32_e32 v238, v238, v136
	v_add_f32_e32 v238, v238, v137
	v_mul_f32_e32 v238, 0x3b000000, v238
	v_max_f32_e32 v238, 0xda24260, v238
	v_rcp_f32_e32 v240, v219
	v_sqrt_f32_e32 v238, v238
	s_nop 0
	v_mul_f32_e32 v238, v240, v238
	v_max_f32_e32 v241, v220, v238
	v_mul_f32_e32 v242, 0x3a83126f, v219
	v_max_f32_e32 v242, 0x358637bd, v242
	v_max_f32_e32 v243, 0x26901d7d, v241
	v_rcp_f32_e32 v243, v243
	s_nop 0
	v_mul_f32_e32 v243, 0x3c23d70a, v243
	v_log_f32_e32 v243, v243
	s_nop 0
	v_mul_f32_e32 v243, 0x3e4ccccd, v243
	v_exp_f32_e32 v243, v243
	s_mov_b32 s52, 0x26901d7d
	v_cmp_ge_f32_e32 vcc, s52, v241
	s_nop 1
	v_cndmask_b32_e32 v243, v243, v242, vcc
	v_mul_f32_e32 v242, 0x42c80000, v219
	v_min3_f32 v1, v242, v243, 1.0
.Lrk_top:
	v_sub_f32_e32 v238, 1.0, v221
	v_min_f32_e32 v178, v1, v238
	v_cmp_eq_f32_e32 vcc, 0, v178
	v_mul_f32_e32 v178, 0x3b000000, v178
	s_cmp_eq_u64 vcc, exec
	s_cbranch_scc1 .Lrk_exit
	s_cmp_gt_i32 s30, 63
	s_cbranch_scc1 .Lrk_exit
	v_mul_f32_e32 v134, 0x3e4ccccd, v173
	v_mul_f32_e32 v142, 0x3e4ccccd, v172
	v_mul_f32_e32 v150, 0x3e4ccccd, v175
	v_mul_f32_e32 v158, 0x3e4ccccd, v174
	v_fma_mixlo_f16 v131, v178, v134, v171
	v_fma_mixlo_f16 v139, v178, v142, v170
	v_fma_mixlo_f16 v147, v178, v150, v169
	v_fma_mixlo_f16 v155, v178, v158, v168
	v_fma_f32 v130, v178, v134, v171
	v_fma_f32 v138, v178, v142, v170
	v_fma_f32 v146, v178, v150, v169
	v_fma_f32 v154, v178, v158, v168
	v_fma_mix_f32 v130, v130, 1.0, -v131 op_sel_hi:[0,0,1]
	v_fma_mix_f32 v138, v138, 1.0, -v139 op_sel_hi:[0,0,1]
	v_fma_mix_f32 v146, v146, 1.0, -v147 op_sel_hi:[0,0,1]
	v_fma_mix_f32 v154, v154, 1.0, -v155 op_sel_hi:[0,0,1]
	v_fma_mixlo_f16 v133, v130, s42, 0
	v_fma_mixlo_f16 v141, v138, s42, 0
	v_fma_mixlo_f16 v149, v146, s42, 0
	v_fma_mixlo_f16 v157, v154, s42, 0
	v_fma_mix_f32 v130, v130, s42, -v133 op_sel_hi:[0,0,1]
	v_fma_mix_f32 v138, v138, s42, -v141 op_sel_hi:[0,0,1]
	v_fma_mix_f32 v146, v146, s42, -v149 op_sel_hi:[0,0,1]
	v_fma_mix_f32 v154, v154, s42, -v157 op_sel_hi:[0,0,1]
	v_fma_mixlo_f16 v132, v130, s42, 0
	v_fma_mixlo_f16 v140, v138, s42, 0
	v_fma_mixlo_f16 v148, v146, s42, 0
	v_fma_mixlo_f16 v156, v154, s42, 0
	ds_write_b16 v204, v131
	ds_write_b16 v205, v139
	ds_write_b16 v206, v147
	ds_write_b16 v207, v155
	ds_write_b16 v204, v133 offset:544
	ds_write_b16 v205, v141 offset:544
	ds_write_b16 v206, v149 offset:544
	ds_write_b16 v207, v157 offset:544
	ds_write_b16 v204, v132 offset:1088
	ds_write_b16 v205, v140 offset:1088
	ds_write_b16 v206, v148 offset:1088
	ds_write_b16 v207, v156 offset:1088
	s_waitcnt lgkmcnt(0)
	s_barrier
	ds_read_b128 v[130:133], v208
	ds_read_b128 v[134:137], v209 offset:64
	ds_read_b128 v[138:141], v211
	ds_read_b128 v[142:145], v212
	ds_read_b128 v[146:149], v213
	ds_read_b128 v[150:153], v214
	ds_read_b128 v[154:157], v215
	ds_read_b128 v[158:161], v216
	s_waitcnt lgkmcnt(7)
	v_smfmac_f32_16x16x64_f16 v[230:233], v[130:133], a[16:23], v210
	ds_read_b128 v[238:241], v217
	ds_read_b128 v[242:245], v217
	v_smfmac_f32_16x16x64_f16 v[234:237], v[130:133], v[180:187], v210
	ds_read_b128 v[180:183], v199 offset:12288
	ds_read_b128 v[184:187], v199 offset:13312
	s_waitcnt lgkmcnt(10)
	v_smfmac_f32_16x16x64_f16 v[230:233], v[134:137], a[48:55], v210
	v_mul_f32_e32 v166, 0x3d99999a, v173
	v_mul_f32_e32 v167, 0x3d99999a, v172
	v_smfmac_f32_16x16x64_f16 v[234:237], v[134:137], v[188:195], v210
	ds_read_b128 v[188:191], v199 offset:16384
	ds_read_b128 v[192:195], v199 offset:17408
	s_waitcnt lgkmcnt(11)
	v_smfmac_f32_16x16x64_f16 v[230:233], v[138:141], a[80:87], v210
	v_mul_f32_e32 v176, 0x3d99999a, v175
	v_mul_f32_e32 v177, 0x3d99999a, v174
	v_smfmac_f32_16x16x64_f16 v[234:237], v[138:141], v[222:229], v210
	ds_read_b128 v[222:225], v199 offset:20480
	ds_read_b128 v[226:229], v199 offset:21504
	s_waitcnt lgkmcnt(12)
	v_smfmac_f32_16x16x64_f16 v[230:233], v[142:145], a[112:119], v210
	s_waitcnt lgkmcnt(4)
	v_smfmac_f32_16x16x64_f16 v[234:237], v[142:145], v[180:187], v210
	ds_read_b128 v[180:183], v199 offset:24576
	ds_read_b128 v[184:187], v199 offset:25600
	v_smfmac_f32_16x16x64_f16 v[230:233], v[146:149], a[144:151], v210
	s_waitcnt lgkmcnt(4)
	v_smfmac_f32_16x16x64_f16 v[234:237], v[146:149], v[188:195], v210
	ds_read_b128 v[188:191], v199 offset:28672
	ds_read_b128 v[192:195], v199 offset:29696
	v_smfmac_f32_16x16x64_f16 v[230:233], v[150:153], a[176:183], v210
	s_waitcnt lgkmcnt(4)
	v_smfmac_f32_16x16x64_f16 v[234:237], v[150:153], v[222:229], v210
	ds_read_b128 v[222:225], v199 offset:2048
	ds_read_b128 v[226:229], v199 offset:3072
	v_smfmac_f32_16x16x64_f16 v[230:233], v[154:157], a[208:215], v210
	s_waitcnt lgkmcnt(4)
	v_smfmac_f32_16x16x64_f16 v[234:237], v[154:157], v[180:187], v210
	ds_read_b128 v[180:183], v199 offset:6144
	ds_read_b128 v[184:187], v199 offset:7168
	v_smfmac_f32_16x16x64_f16 v[230:233], v[158:161], a[240:247], v210
	s_waitcnt lgkmcnt(4)
	v_smfmac_f32_16x16x64_f16 v[234:237], v[158:161], v[188:195], v210
	ds_read_b128 v[188:191], v199 offset:10240
	ds_read_b128 v[192:195], v199 offset:11264
	v_smfmac_f32_16x16x64_f16 v[238:241], v[130:133], a[24:31], v210
	s_waitcnt lgkmcnt(4)
	v_smfmac_f32_16x16x64_f16 v[242:245], v[130:133], v[222:229], v210
	ds_read_b128 v[222:225], v199 offset:14336
	ds_read_b128 v[226:229], v199 offset:15360
	v_smfmac_f32_16x16x64_f16 v[238:241], v[134:137], a[56:63], v210
	v_fmac_f32_e32 v230, s40, v231
	v_fmac_f32_e32 v234, s40, v235
	v_fmac_f32_e32 v230, s41, v232
	s_waitcnt lgkmcnt(4)
	v_smfmac_f32_16x16x64_f16 v[242:245], v[134:137], v[180:187], v210
	ds_read_b128 v[180:183], v199 offset:18432
	ds_read_b128 v[184:187], v199 offset:19456
	v_smfmac_f32_16x16x64_f16 v[238:241], v[138:141], a[88:95], v210
	v_fmac_f32_e32 v234, s41, v236
	s_nop 1
	v_permlane32_swap_b32_e32 v230, v234
	v_add_f32_e32 v164, v230, v234
	s_waitcnt lgkmcnt(4)
	v_smfmac_f32_16x16x64_f16 v[242:245], v[138:141], v[188:195], v210
	ds_read_b128 v[188:191], v199 offset:22528
	ds_read_b128 v[192:195], v199 offset:23552
	v_smfmac_f32_16x16x64_f16 v[238:241], v[142:145], a[120:127], v210
	v_fmac_f32_e32 v176, 0x3e666666, v164
	v_fma_mixlo_f16 v232, v178, v176, v169
	v_fma_f32 v231, v178, v176, v169
	s_waitcnt lgkmcnt(4)
	v_smfmac_f32_16x16x64_f16 v[242:245], v[142:145], v[222:229], v210
	ds_read_b128 v[222:225], v199 offset:26624
	ds_read_b128 v[226:229], v199 offset:27648
	v_smfmac_f32_16x16x64_f16 v[238:241], v[146:149], a[152:159], v210
	v_fma_mix_f32 v231, v231, 1.0, -v232 op_sel_hi:[0,0,1]
	v_fma_mixlo_f16 v235, v231, s42, 0
	v_fma_mix_f32 v231, v231, s42, -v235 op_sel_hi:[0,0,1]
	s_waitcnt lgkmcnt(4)
	v_smfmac_f32_16x16x64_f16 v[242:245], v[146:149], v[180:187], v210
	ds_read_b128 v[180:183], v199 offset:30720
	ds_read_b128 v[184:187], v199 offset:31744
	v_smfmac_f32_16x16x64_f16 v[238:241], v[150:153], a[184:191], v210
	v_fma_mixlo_f16 v233, v231, s42, 0
	ds_write_b16 v206, v232 offset:8704
	s_waitcnt lgkmcnt(5)
	v_smfmac_f32_16x16x64_f16 v[242:245], v[150:153], v[188:195], v210
	v_smfmac_f32_16x16x64_f16 v[238:241], v[154:157], a[216:223], v210
	ds_write_b16 v206, v235 offset:9248
	ds_write_b16 v206, v233 offset:9792
	s_waitcnt lgkmcnt(5)
	v_smfmac_f32_16x16x64_f16 v[242:245], v[154:157], v[222:229], v210
	v_smfmac_f32_16x16x64_f16 v[238:241], v[158:161], a[248:255], v210
	ds_read_b128 v[230:233], v217
	ds_read_b128 v[234:237], v217
	s_waitcnt lgkmcnt(5)
	v_smfmac_f32_16x16x64_f16 v[242:245], v[158:161], v[180:187], v210
	s_waitcnt lgkmcnt(1)
	v_smfmac_f32_16x16x64_f16 v[230:233], v[130:133], a[0:7], v210
	s_waitcnt lgkmcnt(0)
	v_smfmac_f32_16x16x64_f16 v[234:237], v[130:133], v[18:25], v210
	v_smfmac_f32_16x16x64_f16 v[230:233], v[134:137], a[40:47], v210
	v_fmac_f32_e32 v238, s40, v239
	v_fmac_f32_e32 v242, s40, v243
	v_fmac_f32_e32 v238, s41, v240
	v_smfmac_f32_16x16x64_f16 v[234:237], v[134:137], v[34:41], v210
	v_smfmac_f32_16x16x64_f16 v[230:233], v[138:141], a[64:71], v210
	v_fmac_f32_e32 v242, s41, v244
	s_nop 1
	v_permlane32_swap_b32_e32 v238, v242
	v_add_f32_e32 v165, v238, v242
	v_smfmac_f32_16x16x64_f16 v[234:237], v[138:141], v[42:49], v210
	v_smfmac_f32_16x16x64_f16 v[230:233], v[142:145], a[96:103], v210
	v_fmac_f32_e32 v177, 0x3e666666, v165
	v_fma_mixlo_f16 v240, v178, v177, v168
	v_fma_f32 v239, v178, v177, v168
	v_smfmac_f32_16x16x64_f16 v[234:237], v[142:145], v[58:65], v210
	v_smfmac_f32_16x16x64_f16 v[230:233], v[146:149], a[128:135], v210
	v_fma_mix_f32 v239, v239, 1.0, -v240 op_sel_hi:[0,0,1]
	v_fma_mixlo_f16 v243, v239, s42, 0
	v_fma_mix_f32 v239, v239, s42, -v243 op_sel_hi:[0,0,1]
	v_smfmac_f32_16x16x64_f16 v[234:237], v[146:149], v[74:81], v210
	v_smfmac_f32_16x16x64_f16 v[230:233], v[150:153], a[160:167], v210
	v_fma_mixlo_f16 v241, v239, s42, 0
	ds_write_b16 v207, v240 offset:8704
	v_smfmac_f32_16x16x64_f16 v[234:237], v[150:153], v[98:105], v210
	v_smfmac_f32_16x16x64_f16 v[230:233], v[154:157], a[192:199], v210
	ds_write_b16 v207, v243 offset:9248
	ds_write_b16 v207, v241 offset:9792
	v_smfmac_f32_16x16x64_f16 v[234:237], v[154:157], v[106:113], v210
	v_smfmac_f32_16x16x64_f16 v[230:233], v[158:161], a[224:231], v210
	ds_read_b128 v[238:241], v217
	ds_read_b128 v[242:245], v217
	v_smfmac_f32_16x16x64_f16 v[234:237], v[158:161], v[122:129], v210
	s_waitcnt lgkmcnt(1)
	v_smfmac_f32_16x16x64_f16 v[238:241], v[130:133], a[8:15], v210
	s_waitcnt lgkmcnt(0)
	v_smfmac_f32_16x16x64_f16 v[242:245], v[130:133], v[2:9], v210
	v_smfmac_f32_16x16x64_f16 v[238:241], v[134:137], a[32:39], v210
	v_fmac_f32_e32 v230, s40, v231
	v_fmac_f32_e32 v234, s40, v235
	v_fmac_f32_e32 v230, s41, v232
	v_smfmac_f32_16x16x64_f16 v[242:245], v[134:137], v[10:17], v210
	v_smfmac_f32_16x16x64_f16 v[238:241], v[138:141], a[72:79], v210
	v_fmac_f32_e32 v234, s41, v236
	s_nop 1
	v_permlane32_swap_b32_e32 v230, v234
	v_add_f32_e32 v162, v230, v234
	v_smfmac_f32_16x16x64_f16 v[242:245], v[138:141], v[50:57], v210
	v_smfmac_f32_16x16x64_f16 v[238:241], v[142:145], a[104:111], v210
	v_fmac_f32_e32 v166, 0x3e666666, v162
	v_fma_mixlo_f16 v232, v178, v166, v171
	v_fma_f32 v231, v178, v166, v171
	v_smfmac_f32_16x16x64_f16 v[242:245], v[142:145], v[26:33], v210
	v_smfmac_f32_16x16x64_f16 v[238:241], v[146:149], a[136:143], v210
	v_fma_mix_f32 v231, v231, 1.0, -v232 op_sel_hi:[0,0,1]
	v_fma_mixlo_f16 v235, v231, s42, 0
	v_fma_mix_f32 v231, v231, s42, -v235 op_sel_hi:[0,0,1]
	v_smfmac_f32_16x16x64_f16 v[242:245], v[146:149], v[82:89], v210
	v_smfmac_f32_16x16x64_f16 v[238:241], v[150:153], a[168:175], v210
	v_fma_mixlo_f16 v233, v231, s42, 0
	ds_write_b16 v204, v232 offset:8704
	v_smfmac_f32_16x16x64_f16 v[242:245], v[150:153], v[66:73], v210
	v_smfmac_f32_16x16x64_f16 v[238:241], v[154:157], a[200:207], v210
	ds_write_b16 v204, v235 offset:9248
	ds_write_b16 v204, v233 offset:9792
	v_smfmac_f32_16x16x64_f16 v[242:245], v[154:157], v[114:121], v210
	v_smfmac_f32_16x16x64_f16 v[238:241], v[158:161], a[232:239], v210
	ds_read_b128 v[230:233], v217
	ds_read_b128 v[234:237], v217
	v_smfmac_f32_16x16x64_f16 v[242:245], v[158:161], v[90:97], v210
	s_nop 4
	v_fmac_f32_e32 v238, s40, v239
	s_nop 1
	v_fmac_f32_e32 v242, s40, v243
	v_fmac_f32_e32 v238, s41, v240
	v_fmac_f32_e32 v242, s41, v244
	s_nop 1
	v_permlane32_swap_b32_e32 v238, v242
	v_add_f32_e32 v163, v238, v242
	v_fmac_f32_e32 v167, 0x3e666666, v163
	v_fma_mixlo_f16 v240, v178, v167, v170
	v_fma_f32 v239, v178, v167, v170
	v_fma_mix_f32 v239, v239, 1.0, -v240 op_sel_hi:[0,0,1]
	v_fma_mixlo_f16 v243, v239, s42, 0
	v_fma_mix_f32 v239, v239, s42, -v243 op_sel_hi:[0,0,1]
	v_fma_mixlo_f16 v241, v239, s42, 0
	ds_write_b16 v205, v240 offset:8704
	ds_write_b16 v205, v243 offset:9248
	ds_write_b16 v205, v241 offset:9792
	ds_read_b128 v[180:183], v199 offset:0
	ds_read_b128 v[184:187], v199 offset:1024
	ds_read_b128 v[188:191], v199 offset:4096
	ds_read_b128 v[192:195], v199 offset:5120
	ds_read_b128 v[222:225], v199 offset:8192
	s_waitcnt lgkmcnt(6)
	ds_read_b128 v[226:229], v199 offset:9216
	s_waitcnt lgkmcnt(0)
	s_barrier
	ds_read_b128 v[130:133], v208 offset:8704
	ds_read_b128 v[134:137], v209 offset:8768
	ds_read_b128 v[138:141], v211 offset:8704
	ds_read_b128 v[142:145], v212 offset:8704
	ds_read_b128 v[146:149], v213 offset:8704
	ds_read_b128 v[150:153], v214 offset:8704
	ds_read_b128 v[154:157], v215 offset:8704
	ds_read_b128 v[158:161], v216 offset:8704
	s_waitcnt lgkmcnt(7)
	v_smfmac_f32_16x16x64_f16 v[230:233], v[130:133], a[16:23], v210
	ds_read_b128 v[238:241], v217
	ds_read_b128 v[242:245], v217
	v_smfmac_f32_16x16x64_f16 v[234:237], v[130:133], v[180:187], v210
	ds_read_b128 v[180:183], v199 offset:12288
	ds_read_b128 v[184:187], v199 offset:13312
	s_waitcnt lgkmcnt(10)
	v_smfmac_f32_16x16x64_f16 v[230:233], v[134:137], a[48:55], v210
	v_mul_f32_e32 v179, 0x3f7a4fa5, v173
	v_fmac_f32_e32 v179, 0xc06eeeef, v162
	v_smfmac_f32_16x16x64_f16 v[234:237], v[134:137], v[188:195], v210
	ds_read_b128 v[188:191], v199 offset:16384
	ds_read_b128 v[192:195], v199 offset:17408
	s_waitcnt lgkmcnt(11)
	v_smfmac_f32_16x16x64_f16 v[230:233], v[138:141], a[80:87], v210
	v_mul_f32_e32 v196, 0x3f7a4fa5, v172
	v_fmac_f32_e32 v196, 0xc06eeeef, v163
	v_smfmac_f32_16x16x64_f16 v[234:237], v[138:141], v[222:229], v210
	ds_read_b128 v[222:225], v199 offset:20480
	ds_read_b128 v[226:229], v199 offset:21504
	s_waitcnt lgkmcnt(12)
	v_smfmac_f32_16x16x64_f16 v[230:233], v[142:145], a[112:119], v210
	v_mul_f32_e32 v197, 0x3f7a4fa5, v175
	v_fmac_f32_e32 v197, 0xc06eeeef, v164
	s_waitcnt lgkmcnt(4)
	v_smfmac_f32_16x16x64_f16 v[234:237], v[142:145], v[180:187], v210
	ds_read_b128 v[180:183], v199 offset:24576
	ds_read_b128 v[184:187], v199 offset:25600
	v_smfmac_f32_16x16x64_f16 v[230:233], v[146:149], a[144:151], v210
	v_mul_f32_e32 v198, 0x3f7a4fa5, v174
	v_fmac_f32_e32 v198, 0xc06eeeef, v165
	s_waitcnt lgkmcnt(4)
	v_smfmac_f32_16x16x64_f16 v[234:237], v[146:149], v[188:195], v210
	ds_read_b128 v[188:191], v199 offset:28672
	ds_read_b128 v[192:195], v199 offset:29696
	v_smfmac_f32_16x16x64_f16 v[230:233], v[150:153], a[176:183], v210
	s_waitcnt lgkmcnt(4)
	v_smfmac_f32_16x16x64_f16 v[234:237], v[150:153], v[222:229], v210
	ds_read_b128 v[222:225], v199 offset:2048
	ds_read_b128 v[226:229], v199 offset:3072
	v_smfmac_f32_16x16x64_f16 v[230:233], v[154:157], a[208:215], v210
	s_waitcnt lgkmcnt(4)
	v_smfmac_f32_16x16x64_f16 v[234:237], v[154:157], v[180:187], v210
	ds_read_b128 v[180:183], v199 offset:6144
	ds_read_b128 v[184:187], v199 offset:7168
	v_smfmac_f32_16x16x64_f16 v[230:233], v[158:161], a[240:247], v210
	s_waitcnt lgkmcnt(4)
	v_smfmac_f32_16x16x64_f16 v[234:237], v[158:161], v[188:195], v210
	ds_read_b128 v[188:191], v199 offset:10240
	ds_read_b128 v[192:195], v199 offset:11264
	v_smfmac_f32_16x16x64_f16 v[238:241], v[130:133], a[24:31], v210
	s_waitcnt lgkmcnt(4)
	v_smfmac_f32_16x16x64_f16 v[242:245], v[130:133], v[222:229], v210
	ds_read_b128 v[222:225], v199 offset:14336
	ds_read_b128 v[226:229], v199 offset:15360
	v_smfmac_f32_16x16x64_f16 v[238:241], v[134:137], a[56:63], v210
	v_fmac_f32_e32 v230, s40, v231
	v_fmac_f32_e32 v234, s40, v235
	v_fmac_f32_e32 v230, s41, v232
	s_waitcnt lgkmcnt(4)
	v_smfmac_f32_16x16x64_f16 v[242:245], v[134:137], v[180:187], v210
	ds_read_b128 v[180:183], v199 offset:18432
	ds_read_b128 v[184:187], v199 offset:19456
	v_smfmac_f32_16x16x64_f16 v[238:241], v[138:141], a[88:95], v210
	v_fmac_f32_e32 v234, s41, v236
	s_nop 1
	v_permlane32_swap_b32_e32 v230, v234
	v_add_f32_e32 v176, v230, v234
	s_waitcnt lgkmcnt(4)
	v_smfmac_f32_16x16x64_f16 v[242:245], v[138:141], v[188:195], v210
	ds_read_b128 v[188:191], v199 offset:22528
	ds_read_b128 v[192:195], v199 offset:23552
	v_smfmac_f32_16x16x64_f16 v[238:241], v[142:145], a[120:127], v210
	v_fmac_f32_e32 v197, 0x40638e39, v176
	v_fma_mixlo_f16 v232, v178, v197, v169
	v_fma_f32 v231, v178, v197, v169
	s_waitcnt lgkmcnt(4)
	v_smfmac_f32_16x16x64_f16 v[242:245], v[142:145], v[222:229], v210
	ds_read_b128 v[222:225], v199 offset:26624
	ds_read_b128 v[226:229], v199 offset:27648
	v_smfmac_f32_16x16x64_f16 v[238:241], v[146:149], a[152:159], v210
	v_fma_mix_f32 v231, v231, 1.0, -v232 op_sel_hi:[0,0,1]
	v_fma_mixlo_f16 v235, v231, s42, 0
	v_fma_mix_f32 v231, v231, s42, -v235 op_sel_hi:[0,0,1]
	s_waitcnt lgkmcnt(4)
	v_smfmac_f32_16x16x64_f16 v[242:245], v[146:149], v[180:187], v210
	ds_read_b128 v[180:183], v199 offset:30720
	ds_read_b128 v[184:187], v199 offset:31744
	v_smfmac_f32_16x16x64_f16 v[238:241], v[150:153], a[184:191], v210
	v_fma_mixlo_f16 v233, v231, s42, 0
	ds_write_b16 v206, v232
	s_waitcnt lgkmcnt(5)
	v_smfmac_f32_16x16x64_f16 v[242:245], v[150:153], v[188:195], v210
	v_smfmac_f32_16x16x64_f16 v[238:241], v[154:157], a[216:223], v210
	ds_write_b16 v206, v235 offset:544
	ds_write_b16 v206, v233 offset:1088
	s_waitcnt lgkmcnt(5)
	v_smfmac_f32_16x16x64_f16 v[242:245], v[154:157], v[222:229], v210
	v_smfmac_f32_16x16x64_f16 v[238:241], v[158:161], a[248:255], v210
	ds_read_b128 v[230:233], v217
	ds_read_b128 v[234:237], v217
	s_waitcnt lgkmcnt(5)
	v_smfmac_f32_16x16x64_f16 v[242:245], v[158:161], v[180:187], v210
	s_waitcnt lgkmcnt(1)
	v_smfmac_f32_16x16x64_f16 v[230:233], v[130:133], a[0:7], v210
	s_waitcnt lgkmcnt(0)
	v_smfmac_f32_16x16x64_f16 v[234:237], v[130:133], v[18:25], v210
	v_smfmac_f32_16x16x64_f16 v[230:233], v[134:137], a[40:47], v210
	v_fmac_f32_e32 v238, s40, v239
	v_fmac_f32_e32 v242, s40, v243
	v_fmac_f32_e32 v238, s41, v240
	v_smfmac_f32_16x16x64_f16 v[234:237], v[134:137], v[34:41], v210
	v_smfmac_f32_16x16x64_f16 v[230:233], v[138:141], a[64:71], v210
	v_fmac_f32_e32 v242, s41, v244
	s_nop 1
	v_permlane32_swap_b32_e32 v238, v242
	v_add_f32_e32 v177, v238, v242
	v_smfmac_f32_16x16x64_f16 v[234:237], v[138:141], v[42:49], v210
	v_smfmac_f32_16x16x64_f16 v[230:233], v[142:145], a[96:103], v210
	v_fmac_f32_e32 v198, 0x40638e39, v177
	v_fma_mixlo_f16 v240, v178, v198, v168
	v_fma_f32 v239, v178, v198, v168
	v_smfmac_f32_16x16x64_f16 v[234:237], v[142:145], v[58:65], v210
	v_smfmac_f32_16x16x64_f16 v[230:233], v[146:149], a[128:135], v210
	v_fma_mix_f32 v239, v239, 1.0, -v240 op_sel_hi:[0,0,1]
	v_fma_mixlo_f16 v243, v239, s42, 0
	v_fma_mix_f32 v239, v239, s42, -v243 op_sel_hi:[0,0,1]
	v_smfmac_f32_16x16x64_f16 v[234:237], v[146:149], v[74:81], v210
	v_smfmac_f32_16x16x64_f16 v[230:233], v[150:153], a[160:167], v210
	v_fma_mixlo_f16 v241, v239, s42, 0
	ds_write_b16 v207, v240
	v_smfmac_f32_16x16x64_f16 v[234:237], v[150:153], v[98:105], v210
	v_smfmac_f32_16x16x64_f16 v[230:233], v[154:157], a[192:199], v210
	ds_write_b16 v207, v243 offset:544
	ds_write_b16 v207, v241 offset:1088
	v_smfmac_f32_16x16x64_f16 v[234:237], v[154:157], v[106:113], v210
	v_smfmac_f32_16x16x64_f16 v[230:233], v[158:161], a[224:231], v210
	ds_read_b128 v[238:241], v217
	ds_read_b128 v[242:245], v217
	v_smfmac_f32_16x16x64_f16 v[234:237], v[158:161], v[122:129], v210
	s_waitcnt lgkmcnt(1)
	v_smfmac_f32_16x16x64_f16 v[238:241], v[130:133], a[8:15], v210
	s_waitcnt lgkmcnt(0)
	v_smfmac_f32_16x16x64_f16 v[242:245], v[130:133], v[2:9], v210
	v_smfmac_f32_16x16x64_f16 v[238:241], v[134:137], a[32:39], v210
	v_fmac_f32_e32 v230, s40, v231
	v_fmac_f32_e32 v234, s40, v235
	v_fmac_f32_e32 v230, s41, v232
	v_smfmac_f32_16x16x64_f16 v[242:245], v[134:137], v[10:17], v210
	v_smfmac_f32_16x16x64_f16 v[238:241], v[138:141], a[72:79], v210
	v_fmac_f32_e32 v234, s41, v236
	s_nop 1
	v_permlane32_swap_b32_e32 v230, v234
	v_add_f32_e32 v166, v230, v234
	v_smfmac_f32_16x16x64_f16 v[242:245], v[138:141], v[50:57], v210
	v_smfmac_f32_16x16x64_f16 v[238:241], v[142:145], a[104:111], v210
	v_fmac_f32_e32 v179, 0x40638e39, v166
	v_fma_mixlo_f16 v232, v178, v179, v171
	v_fma_f32 v231, v178, v179, v171
	v_smfmac_f32_16x16x64_f16 v[242:245], v[142:145], v[26:33], v210
	v_smfmac_f32_16x16x64_f16 v[238:241], v[146:149], a[136:143], v210
	v_fma_mix_f32 v231, v231, 1.0, -v232 op_sel_hi:[0,0,1]
	v_fma_mixlo_f16 v235, v231, s42, 0
	v_fma_mix_f32 v231, v231, s42, -v235 op_sel_hi:[0,0,1]
	v_smfmac_f32_16x16x64_f16 v[242:245], v[146:149], v[82:89], v210
	v_smfmac_f32_16x16x64_f16 v[238:241], v[150:153], a[168:175], v210
	v_fma_mixlo_f16 v233, v231, s42, 0
	ds_write_b16 v204, v232
	v_smfmac_f32_16x16x64_f16 v[242:245], v[150:153], v[66:73], v210
	v_smfmac_f32_16x16x64_f16 v[238:241], v[154:157], a[200:207], v210
	ds_write_b16 v204, v235 offset:544
	ds_write_b16 v204, v233 offset:1088
	v_smfmac_f32_16x16x64_f16 v[242:245], v[154:157], v[114:121], v210
	v_smfmac_f32_16x16x64_f16 v[238:241], v[158:161], a[232:239], v210
	ds_read_b128 v[230:233], v217
	ds_read_b128 v[234:237], v217
	v_smfmac_f32_16x16x64_f16 v[242:245], v[158:161], v[90:97], v210
	s_nop 4
	v_fmac_f32_e32 v238, s40, v239
	s_nop 1
	v_fmac_f32_e32 v242, s40, v243
	v_fmac_f32_e32 v238, s41, v240
	v_fmac_f32_e32 v242, s41, v244
	s_nop 1
	v_permlane32_swap_b32_e32 v238, v242
	v_add_f32_e32 v167, v238, v242
	v_fmac_f32_e32 v196, 0x40638e39, v167
	v_fma_mixlo_f16 v240, v178, v196, v170
	v_fma_f32 v239, v178, v196, v170
	v_fma_mix_f32 v239, v239, 1.0, -v240 op_sel_hi:[0,0,1]
	v_fma_mixlo_f16 v243, v239, s42, 0
	v_fma_mix_f32 v239, v239, s42, -v243 op_sel_hi:[0,0,1]
	v_fma_mixlo_f16 v241, v239, s42, 0
	ds_write_b16 v205, v240
	ds_write_b16 v205, v243 offset:544
	ds_write_b16 v205, v241 offset:1088
	ds_read_b128 v[180:183], v199 offset:0
	ds_read_b128 v[184:187], v199 offset:1024
	ds_read_b128 v[188:191], v199 offset:4096
	ds_read_b128 v[192:195], v199 offset:5120
	ds_read_b128 v[222:225], v199 offset:8192
	s_waitcnt lgkmcnt(6)
	ds_read_b128 v[226:229], v199 offset:9216
	s_waitcnt lgkmcnt(0)
	s_barrier
	ds_read_b128 v[130:133], v208
	ds_read_b128 v[134:137], v209 offset:64
	ds_read_b128 v[138:141], v211
	ds_read_b128 v[142:145], v212
	ds_read_b128 v[146:149], v213
	ds_read_b128 v[150:153], v214
	ds_read_b128 v[154:157], v215
	ds_read_b128 v[158:161], v216
	s_waitcnt lgkmcnt(7)
	v_smfmac_f32_16x16x64_f16 v[230:233], v[130:133], a[16:23], v210
	ds_read_b128 v[238:241], v217
	ds_read_b128 v[242:245], v217
	v_smfmac_f32_16x16x64_f16 v[234:237], v[130:133], v[180:187], v210
	ds_read_b128 v[180:183], v199 offset:12288
	ds_read_b128 v[184:187], v199 offset:13312
	s_waitcnt lgkmcnt(10)
	v_smfmac_f32_16x16x64_f16 v[230:233], v[134:137], a[48:55], v210
	v_mul_f32_e32 v219, 0x403cf760, v173
	v_fmac_f32_e32 v219, 0xc139885f, v162
	v_smfmac_f32_16x16x64_f16 v[234:237], v[134:137], v[188:195], v210
	ds_read_b128 v[188:191], v199 offset:16384
	ds_read_b128 v[192:195], v199 offset:17408
	s_waitcnt lgkmcnt(11)
	v_smfmac_f32_16x16x64_f16 v[230:233], v[138:141], a[80:87], v210
	v_fmac_f32_e32 v219, 0x411d2a92, v166
	v_mul_f32_e32 v220, 0x403cf760, v172
	v_smfmac_f32_16x16x64_f16 v[234:237], v[138:141], v[222:229], v210
	ds_read_b128 v[222:225], v199 offset:20480
	ds_read_b128 v[226:229], v199 offset:21504
	s_waitcnt lgkmcnt(12)
	v_smfmac_f32_16x16x64_f16 v[230:233], v[142:145], a[112:119], v210
	v_fmac_f32_e32 v220, 0xc139885f, v163
	v_fmac_f32_e32 v220, 0x411d2a92, v167
	s_waitcnt lgkmcnt(4)
	v_smfmac_f32_16x16x64_f16 v[234:237], v[142:145], v[180:187], v210
	ds_read_b128 v[180:183], v199 offset:24576
	ds_read_b128 v[184:187], v199 offset:25600
	v_smfmac_f32_16x16x64_f16 v[230:233], v[146:149], a[144:151], v210
	v_mul_f32_e32 v246, 0x403cf760, v175
	v_fmac_f32_e32 v246, 0xc139885f, v164
	s_waitcnt lgkmcnt(4)
	v_smfmac_f32_16x16x64_f16 v[234:237], v[146:149], v[188:195], v210
	ds_read_b128 v[188:191], v199 offset:28672
	ds_read_b128 v[192:195], v199 offset:29696
	v_smfmac_f32_16x16x64_f16 v[230:233], v[150:153], a[176:183], v210
	v_fmac_f32_e32 v246, 0x411d2a92, v176
	v_mul_f32_e32 v247, 0x403cf760, v174
	s_waitcnt lgkmcnt(4)
	v_smfmac_f32_16x16x64_f16 v[234:237], v[150:153], v[222:229], v210
	ds_read_b128 v[222:225], v199 offset:2048
	ds_read_b128 v[226:229], v199 offset:3072
	v_smfmac_f32_16x16x64_f16 v[230:233], v[154:157], a[208:215], v210
	v_fmac_f32_e32 v247, 0xc139885f, v165
	v_fmac_f32_e32 v247, 0x411d2a92, v177
	s_waitcnt lgkmcnt(4)
	v_smfmac_f32_16x16x64_f16 v[234:237], v[154:157], v[180:187], v210
	ds_read_b128 v[180:183], v199 offset:6144
	ds_read_b128 v[184:187], v199 offset:7168
	v_smfmac_f32_16x16x64_f16 v[230:233], v[158:161], a[240:247], v210
	s_waitcnt lgkmcnt(4)
	v_smfmac_f32_16x16x64_f16 v[234:237], v[158:161], v[188:195], v210
	ds_read_b128 v[188:191], v199 offset:10240
	ds_read_b128 v[192:195], v199 offset:11264
	v_smfmac_f32_16x16x64_f16 v[238:241], v[130:133], a[24:31], v210
	s_waitcnt lgkmcnt(4)
	v_smfmac_f32_16x16x64_f16 v[242:245], v[130:133], v[222:229], v210
	ds_read_b128 v[222:225], v199 offset:14336
	ds_read_b128 v[226:229], v199 offset:15360
	v_smfmac_f32_16x16x64_f16 v[238:241], v[134:137], a[56:63], v210
	v_fmac_f32_e32 v230, s40, v231
	v_fmac_f32_e32 v234, s40, v235
	v_fmac_f32_e32 v230, s41, v232
	s_waitcnt lgkmcnt(4)
	v_smfmac_f32_16x16x64_f16 v[242:245], v[134:137], v[180:187], v210
	ds_read_b128 v[180:183], v199 offset:18432
	ds_read_b128 v[184:187], v199 offset:19456
	v_smfmac_f32_16x16x64_f16 v[238:241], v[138:141], a[88:95], v210
	v_fmac_f32_e32 v234, s41, v236
	s_nop 1
	v_permlane32_swap_b32_e32 v230, v234
	v_add_f32_e32 v197, v230, v234
	s_waitcnt lgkmcnt(4)
	v_smfmac_f32_16x16x64_f16 v[242:245], v[138:141], v[188:195], v210
	ds_read_b128 v[188:191], v199 offset:22528
	ds_read_b128 v[192:195], v199 offset:23552
	v_smfmac_f32_16x16x64_f16 v[238:241], v[142:145], a[120:127], v210
	v_fmac_f32_e32 v246, 0xbe94e4f6, v197
	v_fma_mixlo_f16 v232, v178, v246, v169
	v_fma_f32 v231, v178, v246, v169
	s_waitcnt lgkmcnt(4)
	v_smfmac_f32_16x16x64_f16 v[242:245], v[142:145], v[222:229], v210
	ds_read_b128 v[222:225], v199 offset:26624
	ds_read_b128 v[226:229], v199 offset:27648
	v_smfmac_f32_16x16x64_f16 v[238:241], v[146:149], a[152:159], v210
	v_fma_mix_f32 v231, v231, 1.0, -v232 op_sel_hi:[0,0,1]
	v_fma_mixlo_f16 v235, v231, s42, 0
	v_fma_mix_f32 v231, v231, s42, -v235 op_sel_hi:[0,0,1]
	s_waitcnt lgkmcnt(4)
	v_smfmac_f32_16x16x64_f16 v[242:245], v[146:149], v[180:187], v210
	ds_read_b128 v[180:183], v199 offset:30720
	ds_read_b128 v[184:187], v199 offset:31744
	v_smfmac_f32_16x16x64_f16 v[238:241], v[150:153], a[184:191], v210
	v_fma_mixlo_f16 v233, v231, s42, 0
	ds_write_b16 v206, v232 offset:8704
	s_waitcnt lgkmcnt(5)
	v_smfmac_f32_16x16x64_f16 v[242:245], v[150:153], v[188:195], v210
	v_smfmac_f32_16x16x64_f16 v[238:241], v[154:157], a[216:223], v210
	ds_write_b16 v206, v235 offset:9248
	ds_write_b16 v206, v233 offset:9792
	s_waitcnt lgkmcnt(5)
	v_smfmac_f32_16x16x64_f16 v[242:245], v[154:157], v[222:229], v210
	v_smfmac_f32_16x16x64_f16 v[238:241], v[158:161], a[248:255], v210
	ds_read_b128 v[230:233], v217
	ds_read_b128 v[234:237], v217
	s_waitcnt lgkmcnt(5)
	v_smfmac_f32_16x16x64_f16 v[242:245], v[158:161], v[180:187], v210
	s_waitcnt lgkmcnt(1)
	v_smfmac_f32_16x16x64_f16 v[230:233], v[130:133], a[0:7], v210
	s_waitcnt lgkmcnt(0)
	v_smfmac_f32_16x16x64_f16 v[234:237], v[130:133], v[18:25], v210
	v_smfmac_f32_16x16x64_f16 v[230:233], v[134:137], a[40:47], v210
	v_fmac_f32_e32 v238, s40, v239
	v_fmac_f32_e32 v242, s40, v243
	v_fmac_f32_e32 v238, s41, v240
	v_smfmac_f32_16x16x64_f16 v[234:237], v[134:137], v[34:41], v210
	v_smfmac_f32_16x16x64_f16 v[230:233], v[138:141], a[64:71], v210
	v_fmac_f32_e32 v242, s41, v244
	s_nop 1
	v_permlane32_swap_b32_e32 v238, v242
	v_add_f32_e32 v198, v238, v242
	v_smfmac_f32_16x16x64_f16 v[234:237], v[138:141], v[42:49], v210
	v_smfmac_f32_16x16x64_f16 v[230:233], v[142:145], a[96:103], v210
	v_fmac_f32_e32 v247, 0xbe94e4f6, v198
	v_fma_mixlo_f16 v240, v178, v247, v168
	v_fma_f32 v239, v178, v247, v168
	v_smfmac_f32_16x16x64_f16 v[234:237], v[142:145], v[58:65], v210
	v_smfmac_f32_16x16x64_f16 v[230:233], v[146:149], a[128:135], v210
	v_fma_mix_f32 v239, v239, 1.0, -v240 op_sel_hi:[0,0,1]
	v_fma_mixlo_f16 v243, v239, s42, 0
	v_fma_mix_f32 v239, v239, s42, -v243 op_sel_hi:[0,0,1]
	v_smfmac_f32_16x16x64_f16 v[234:237], v[146:149], v[74:81], v210
	v_smfmac_f32_16x16x64_f16 v[230:233], v[150:153], a[160:167], v210
	v_fma_mixlo_f16 v241, v239, s42, 0
	ds_write_b16 v207, v240 offset:8704
	v_smfmac_f32_16x16x64_f16 v[234:237], v[150:153], v[98:105], v210
	v_smfmac_f32_16x16x64_f16 v[230:233], v[154:157], a[192:199], v210
	ds_write_b16 v207, v243 offset:9248
	ds_write_b16 v207, v241 offset:9792
	v_smfmac_f32_16x16x64_f16 v[234:237], v[154:157], v[106:113], v210
	v_smfmac_f32_16x16x64_f16 v[230:233], v[158:161], a[224:231], v210
	ds_read_b128 v[238:241], v217
	ds_read_b128 v[242:245], v217
	v_smfmac_f32_16x16x64_f16 v[234:237], v[158:161], v[122:129], v210
	s_waitcnt lgkmcnt(1)
	v_smfmac_f32_16x16x64_f16 v[238:241], v[130:133], a[8:15], v210
	s_waitcnt lgkmcnt(0)
	v_smfmac_f32_16x16x64_f16 v[242:245], v[130:133], v[2:9], v210
	v_smfmac_f32_16x16x64_f16 v[238:241], v[134:137], a[32:39], v210
	v_fmac_f32_e32 v230, s40, v231
	v_fmac_f32_e32 v234, s40, v235
	v_fmac_f32_e32 v230, s41, v232
	v_smfmac_f32_16x16x64_f16 v[242:245], v[134:137], v[10:17], v210
	v_smfmac_f32_16x16x64_f16 v[238:241], v[138:141], a[72:79], v210
	v_fmac_f32_e32 v234, s41, v236
	s_nop 1
	v_permlane32_swap_b32_e32 v230, v234
	v_add_f32_e32 v179, v230, v234
	v_smfmac_f32_16x16x64_f16 v[242:245], v[138:141], v[50:57], v210
	v_smfmac_f32_16x16x64_f16 v[238:241], v[142:145], a[104:111], v210
	v_fmac_f32_e32 v219, 0xbe94e4f6, v179
	v_fma_mixlo_f16 v232, v178, v219, v171
	v_fma_f32 v231, v178, v219, v171
	v_smfmac_f32_16x16x64_f16 v[242:245], v[142:145], v[26:33], v210
	v_smfmac_f32_16x16x64_f16 v[238:241], v[146:149], a[136:143], v210
	v_fma_mix_f32 v231, v231, 1.0, -v232 op_sel_hi:[0,0,1]
	v_fma_mixlo_f16 v235, v231, s42, 0
	v_fma_mix_f32 v231, v231, s42, -v235 op_sel_hi:[0,0,1]
	v_smfmac_f32_16x16x64_f16 v[242:245], v[146:149], v[82:89], v210
	v_smfmac_f32_16x16x64_f16 v[238:241], v[150:153], a[168:175], v210
	v_fma_mixlo_f16 v233, v231, s42, 0
	ds_write_b16 v204, v232 offset:8704
	v_smfmac_f32_16x16x64_f16 v[242:245], v[150:153], v[66:73], v210
	v_smfmac_f32_16x16x64_f16 v[238:241], v[154:157], a[200:207], v210
	ds_write_b16 v204, v235 offset:9248
	ds_write_b16 v204, v233 offset:9792
	v_smfmac_f32_16x16x64_f16 v[242:245], v[154:157], v[114:121], v210
	v_smfmac_f32_16x16x64_f16 v[238:241], v[158:161], a[232:239], v210
	ds_read_b128 v[230:233], v217
	ds_read_b128 v[234:237], v217
	v_smfmac_f32_16x16x64_f16 v[242:245], v[158:161], v[90:97], v210
	s_nop 4
	v_fmac_f32_e32 v238, s40, v239
	s_nop 1
	v_fmac_f32_e32 v242, s40, v243
	v_fmac_f32_e32 v238, s41, v240
	v_fmac_f32_e32 v242, s41, v244
	s_nop 1
	v_permlane32_swap_b32_e32 v238, v242
	v_add_f32_e32 v196, v238, v242
	v_fmac_f32_e32 v220, 0xbe94e4f6, v196
	v_fma_mixlo_f16 v240, v178, v220, v170
	v_fma_f32 v239, v178, v220, v170
	v_fma_mix_f32 v239, v239, 1.0, -v240 op_sel_hi:[0,0,1]
	v_fma_mixlo_f16 v243, v239, s42, 0
	v_fma_mix_f32 v239, v239, s42, -v243 op_sel_hi:[0,0,1]
	v_fma_mixlo_f16 v241, v239, s42, 0
	ds_write_b16 v205, v240 offset:8704
	ds_write_b16 v205, v243 offset:9248
	ds_write_b16 v205, v241 offset:9792
	ds_read_b128 v[180:183], v199 offset:0
	ds_read_b128 v[184:187], v199 offset:1024
	ds_read_b128 v[188:191], v199 offset:4096
	ds_read_b128 v[192:195], v199 offset:5120
	ds_read_b128 v[222:225], v199 offset:8192
	s_waitcnt lgkmcnt(6)
	ds_read_b128 v[226:229], v199 offset:9216
	s_waitcnt lgkmcnt(0)
	s_barrier
	ds_read_b128 v[130:133], v208 offset:8704
	ds_read_b128 v[134:137], v209 offset:8768
	ds_read_b128 v[138:141], v211 offset:8704
	ds_read_b128 v[142:145], v212 offset:8704
	ds_read_b128 v[146:149], v213 offset:8704
	ds_read_b128 v[150:153], v214 offset:8704
	ds_read_b128 v[154:157], v215 offset:8704
	ds_read_b128 v[158:161], v216 offset:8704
	s_waitcnt lgkmcnt(7)
	v_smfmac_f32_16x16x64_f16 v[230:233], v[130:133], a[16:23], v210
	ds_read_b128 v[238:241], v217
	ds_read_b128 v[242:245], v217
	v_mul_f32_e32 v248, 0x40362960, v173
	v_smfmac_f32_16x16x64_f16 v[234:237], v[130:133], v[180:187], v210
	ds_read_b128 v[180:183], v199 offset:12288
	ds_read_b128 v[184:187], v199 offset:13312
	s_waitcnt lgkmcnt(10)
	v_smfmac_f32_16x16x64_f16 v[230:233], v[134:137], a[48:55], v210
	v_fmac_f32_e32 v248, 0xc12c1f08, v162
	v_fmac_f32_e32 v248, 0x410e80b5, v166
	v_fmac_f32_e32 v248, 0x3e8e8ba3, v179
	v_smfmac_f32_16x16x64_f16 v[234:237], v[134:137], v[188:195], v210
	ds_read_b128 v[188:191], v199 offset:16384
	ds_read_b128 v[192:195], v199 offset:17408
	s_waitcnt lgkmcnt(11)
	v_smfmac_f32_16x16x64_f16 v[230:233], v[138:141], a[80:87], v210
	v_mul_f32_e32 v249, 0x40362960, v172
	v_fmac_f32_e32 v249, 0xc12c1f08, v163
	v_smfmac_f32_16x16x64_f16 v[234:237], v[138:141], v[222:229], v210
	ds_read_b128 v[222:225], v199 offset:20480
	ds_read_b128 v[226:229], v199 offset:21504
	s_waitcnt lgkmcnt(12)
	v_smfmac_f32_16x16x64_f16 v[230:233], v[142:145], a[112:119], v210
	v_fmac_f32_e32 v249, 0x410e80b5, v167
	v_fmac_f32_e32 v249, 0x3e8e8ba3, v196
	s_waitcnt lgkmcnt(4)
	v_smfmac_f32_16x16x64_f16 v[234:237], v[142:145], v[180:187], v210
	ds_read_b128 v[180:183], v199 offset:24576
	ds_read_b128 v[184:187], v199 offset:25600
	v_smfmac_f32_16x16x64_f16 v[230:233], v[146:149], a[144:151], v210
	v_mul_f32_e32 v250, 0x40362960, v175
	v_fmac_f32_e32 v250, 0xc12c1f08, v164
	s_waitcnt lgkmcnt(4)
	v_smfmac_f32_16x16x64_f16 v[234:237], v[146:149], v[188:195], v210
	ds_read_b128 v[188:191], v199 offset:28672
	ds_read_b128 v[192:195], v199 offset:29696
	v_smfmac_f32_16x16x64_f16 v[230:233], v[150:153], a[176:183], v210
	v_fmac_f32_e32 v250, 0x410e80b5, v176
	v_fmac_f32_e32 v250, 0x3e8e8ba3, v197
	s_waitcnt lgkmcnt(4)
	v_smfmac_f32_16x16x64_f16 v[234:237], v[150:153], v[222:229], v210
	ds_read_b128 v[222:225], v199 offset:2048
	ds_read_b128 v[226:229], v199 offset:3072
	v_smfmac_f32_16x16x64_f16 v[230:233], v[154:157], a[208:215], v210
	v_mul_f32_e32 v251, 0x40362960, v174
	v_fmac_f32_e32 v251, 0xc12c1f08, v165
	s_waitcnt lgkmcnt(4)
	v_smfmac_f32_16x16x64_f16 v[234:237], v[154:157], v[180:187], v210
	ds_read_b128 v[180:183], v199 offset:6144
	ds_read_b128 v[184:187], v199 offset:7168
	v_smfmac_f32_16x16x64_f16 v[230:233], v[158:161], a[240:247], v210
	v_fmac_f32_e32 v251, 0x410e80b5, v177
	v_fmac_f32_e32 v251, 0x3e8e8ba3, v198
	s_waitcnt lgkmcnt(4)
	v_smfmac_f32_16x16x64_f16 v[234:237], v[158:161], v[188:195], v210
	ds_read_b128 v[188:191], v199 offset:10240
	ds_read_b128 v[192:195], v199 offset:11264
	v_smfmac_f32_16x16x64_f16 v[238:241], v[130:133], a[24:31], v210
	s_waitcnt lgkmcnt(4)
	v_smfmac_f32_16x16x64_f16 v[242:245], v[130:133], v[222:229], v210
	ds_read_b128 v[222:225], v199 offset:14336
	ds_read_b128 v[226:229], v199 offset:15360
	v_smfmac_f32_16x16x64_f16 v[238:241], v[134:137], a[56:63], v210
	v_fmac_f32_e32 v230, s40, v231
	v_fmac_f32_e32 v234, s40, v235
	v_fmac_f32_e32 v230, s41, v232
	s_waitcnt lgkmcnt(4)
	v_smfmac_f32_16x16x64_f16 v[242:245], v[134:137], v[180:187], v210
	ds_read_b128 v[180:183], v199 offset:18432
	ds_read_b128 v[184:187], v199 offset:19456
	v_smfmac_f32_16x16x64_f16 v[238:241], v[138:141], a[88:95], v210
	v_fmac_f32_e32 v234, s41, v236
	s_nop 1
	v_permlane32_swap_b32_e32 v230, v234
	v_add_f32_e32 v246, v230, v234
	s_waitcnt lgkmcnt(4)
	v_smfmac_f32_16x16x64_f16 v[242:245], v[138:141], v[188:195], v210
	ds_read_b128 v[188:191], v199 offset:22528
	ds_read_b128 v[192:195], v199 offset:23552
	v_smfmac_f32_16x16x64_f16 v[238:241], v[142:145], a[120:127], v210
	v_fmac_f32_e32 v250, 0xbe8c0c4c, v246
	v_fma_mixlo_f16 v232, v178, v250, v169
	v_fma_f32 v231, v178, v250, v169
	s_waitcnt lgkmcnt(4)
	v_smfmac_f32_16x16x64_f16 v[242:245], v[142:145], v[222:229], v210
	ds_read_b128 v[222:225], v199 offset:26624
	ds_read_b128 v[226:229], v199 offset:27648
	v_smfmac_f32_16x16x64_f16 v[238:241], v[146:149], a[152:159], v210
	v_fma_mix_f32 v231, v231, 1.0, -v232 op_sel_hi:[0,0,1]
	v_fma_mixlo_f16 v235, v231, s42, 0
	v_fma_mix_f32 v231, v231, s42, -v235 op_sel_hi:[0,0,1]
	s_waitcnt lgkmcnt(4)
	v_smfmac_f32_16x16x64_f16 v[242:245], v[146:149], v[180:187], v210
	ds_read_b128 v[180:183], v199 offset:30720
	ds_read_b128 v[184:187], v199 offset:31744
	v_smfmac_f32_16x16x64_f16 v[238:241], v[150:153], a[184:191], v210
	v_fma_mixlo_f16 v233, v231, s42, 0
	ds_write_b16 v206, v232
	s_waitcnt lgkmcnt(5)
	v_smfmac_f32_16x16x64_f16 v[242:245], v[150:153], v[188:195], v210
	v_smfmac_f32_16x16x64_f16 v[238:241], v[154:157], a[216:223], v210
	ds_write_b16 v206, v235 offset:544
	ds_write_b16 v206, v233 offset:1088
	s_waitcnt lgkmcnt(5)
	v_smfmac_f32_16x16x64_f16 v[242:245], v[154:157], v[222:229], v210
	v_smfmac_f32_16x16x64_f16 v[238:241], v[158:161], a[248:255], v210
	ds_read_b128 v[230:233], v217
	ds_read_b128 v[234:237], v217
	s_waitcnt lgkmcnt(5)
	v_smfmac_f32_16x16x64_f16 v[242:245], v[158:161], v[180:187], v210
	s_waitcnt lgkmcnt(1)
	v_smfmac_f32_16x16x64_f16 v[230:233], v[130:133], a[0:7], v210
	s_waitcnt lgkmcnt(0)
	v_smfmac_f32_16x16x64_f16 v[234:237], v[130:133], v[18:25], v210
	v_smfmac_f32_16x16x64_f16 v[230:233], v[134:137], a[40:47], v210
	v_fmac_f32_e32 v238, s40, v239
	v_fmac_f32_e32 v242, s40, v243
	v_fmac_f32_e32 v238, s41, v240
	v_smfmac_f32_16x16x64_f16 v[234:237], v[134:137], v[34:41], v210
	v_smfmac_f32_16x16x64_f16 v[230:233], v[138:141], a[64:71], v210
	v_fmac_f32_e32 v242, s41, v244
	s_nop 1
	v_permlane32_swap_b32_e32 v238, v242
	v_add_f32_e32 v247, v238, v242
	v_smfmac_f32_16x16x64_f16 v[234:237], v[138:141], v[42:49], v210
	v_smfmac_f32_16x16x64_f16 v[230:233], v[142:145], a[96:103], v210
	v_fmac_f32_e32 v251, 0xbe8c0c4c, v247
	v_fma_mixlo_f16 v240, v178, v251, v168
	v_fma_f32 v239, v178, v251, v168
	v_smfmac_f32_16x16x64_f16 v[234:237], v[142:145], v[58:65], v210
	v_smfmac_f32_16x16x64_f16 v[230:233], v[146:149], a[128:135], v210
	v_fma_mix_f32 v239, v239, 1.0, -v240 op_sel_hi:[0,0,1]
	v_fma_mixlo_f16 v243, v239, s42, 0
	v_fma_mix_f32 v239, v239, s42, -v243 op_sel_hi:[0,0,1]
	v_smfmac_f32_16x16x64_f16 v[234:237], v[146:149], v[74:81], v210
	v_smfmac_f32_16x16x64_f16 v[230:233], v[150:153], a[160:167], v210
	v_fma_mixlo_f16 v241, v239, s42, 0
	ds_write_b16 v207, v240
	v_smfmac_f32_16x16x64_f16 v[234:237], v[150:153], v[98:105], v210
	v_smfmac_f32_16x16x64_f16 v[230:233], v[154:157], a[192:199], v210
	ds_write_b16 v207, v243 offset:544
	ds_write_b16 v207, v241 offset:1088
	v_smfmac_f32_16x16x64_f16 v[234:237], v[154:157], v[106:113], v210
	v_smfmac_f32_16x16x64_f16 v[230:233], v[158:161], a[224:231], v210
	ds_read_b128 v[238:241], v217
	ds_read_b128 v[242:245], v217
	v_smfmac_f32_16x16x64_f16 v[234:237], v[158:161], v[122:129], v210
	s_waitcnt lgkmcnt(1)
	v_smfmac_f32_16x16x64_f16 v[238:241], v[130:133], a[8:15], v210
	s_waitcnt lgkmcnt(0)
	v_smfmac_f32_16x16x64_f16 v[242:245], v[130:133], v[2:9], v210
	v_smfmac_f32_16x16x64_f16 v[238:241], v[134:137], a[32:39], v210
	v_fmac_f32_e32 v230, s40, v231
	v_fmac_f32_e32 v234, s40, v235
	v_fmac_f32_e32 v230, s41, v232
	v_smfmac_f32_16x16x64_f16 v[242:245], v[134:137], v[10:17], v210
	v_smfmac_f32_16x16x64_f16 v[238:241], v[138:141], a[72:79], v210
	v_fmac_f32_e32 v234, s41, v236
	s_nop 1
	v_permlane32_swap_b32_e32 v230, v234
	v_add_f32_e32 v219, v230, v234
	v_smfmac_f32_16x16x64_f16 v[242:245], v[138:141], v[50:57], v210
	v_smfmac_f32_16x16x64_f16 v[238:241], v[142:145], a[104:111], v210
	v_fmac_f32_e32 v248, 0xbe8c0c4c, v219
	v_fma_mixlo_f16 v232, v178, v248, v171
	v_fma_f32 v231, v178, v248, v171
	v_smfmac_f32_16x16x64_f16 v[242:245], v[142:145], v[26:33], v210
	v_smfmac_f32_16x16x64_f16 v[238:241], v[146:149], a[136:143], v210
	v_fma_mix_f32 v231, v231, 1.0, -v232 op_sel_hi:[0,0,1]
	v_fma_mixlo_f16 v235, v231, s42, 0
	v_fma_mix_f32 v231, v231, s42, -v235 op_sel_hi:[0,0,1]
	v_smfmac_f32_16x16x64_f16 v[242:245], v[146:149], v[82:89], v210
	v_smfmac_f32_16x16x64_f16 v[238:241], v[150:153], a[168:175], v210
	v_fma_mixlo_f16 v233, v231, s42, 0
	ds_write_b16 v204, v232
	v_smfmac_f32_16x16x64_f16 v[242:245], v[150:153], v[66:73], v210
	v_smfmac_f32_16x16x64_f16 v[238:241], v[154:157], a[200:207], v210
	ds_write_b16 v204, v235 offset:544
	ds_write_b16 v204, v233 offset:1088
	v_smfmac_f32_16x16x64_f16 v[242:245], v[154:157], v[114:121], v210
	v_smfmac_f32_16x16x64_f16 v[238:241], v[158:161], a[232:239], v210
	ds_read_b128 v[230:233], v217
	ds_read_b128 v[234:237], v217
	v_smfmac_f32_16x16x64_f16 v[242:245], v[158:161], v[90:97], v210
	s_nop 4
	v_fmac_f32_e32 v238, s40, v239
	s_nop 1
	v_fmac_f32_e32 v242, s40, v243
	v_fmac_f32_e32 v238, s41, v240
	v_fmac_f32_e32 v242, s41, v244
	s_nop 1
	v_permlane32_swap_b32_e32 v238, v242
	v_add_f32_e32 v220, v238, v242
	v_fmac_f32_e32 v249, 0xbe8c0c4c, v220
	v_fma_mixlo_f16 v240, v178, v249, v170
	v_fma_f32 v239, v178, v249, v170
	v_fma_mix_f32 v239, v239, 1.0, -v240 op_sel_hi:[0,0,1]
	v_fma_mixlo_f16 v243, v239, s42, 0
	v_fma_mix_f32 v239, v239, s42, -v243 op_sel_hi:[0,0,1]
	v_fma_mixlo_f16 v241, v239, s42, 0
	ds_write_b16 v205, v240
	ds_write_b16 v205, v243 offset:544
	ds_write_b16 v205, v241 offset:1088
	ds_read_b128 v[180:183], v199 offset:0
	ds_read_b128 v[184:187], v199 offset:1024
	ds_read_b128 v[188:191], v199 offset:4096
	ds_read_b128 v[192:195], v199 offset:5120
	ds_read_b128 v[222:225], v199 offset:8192
	s_waitcnt lgkmcnt(6)
	ds_read_b128 v[226:229], v199 offset:9216
	s_waitcnt lgkmcnt(0)
	s_barrier
	ds_read_b128 v[130:133], v208
	ds_read_b128 v[134:137], v209 offset:64
	ds_read_b128 v[138:141], v211
	ds_read_b128 v[142:145], v212
	ds_read_b128 v[146:149], v213
	ds_read_b128 v[150:153], v214
	ds_read_b128 v[154:157], v215
	ds_read_b128 v[158:161], v216
	s_waitcnt lgkmcnt(7)
	v_smfmac_f32_16x16x64_f16 v[230:233], v[130:133], a[16:23], v210
	ds_read_b128 v[238:241], v217
	ds_read_b128 v[242:245], v217
	v_mul_f32_e32 v252, 0x3dbaaaab, v173
	v_smfmac_f32_16x16x64_f16 v[234:237], v[130:133], v[180:187], v210
	ds_read_b128 v[180:183], v199 offset:12288
	ds_read_b128 v[184:187], v199 offset:13312
	s_waitcnt lgkmcnt(10)
	v_smfmac_f32_16x16x64_f16 v[230:233], v[134:137], a[48:55], v210
	v_fmac_f32_e32 v252, 0x3ee6024d, v166
	v_fmac_f32_e32 v252, 0x3f26aaab, v179
	v_fmac_f32_e32 v252, 0xbea50e7e, v219
	v_smfmac_f32_16x16x64_f16 v[234:237], v[134:137], v[188:195], v210
	ds_read_b128 v[188:191], v199 offset:16384
	ds_read_b128 v[192:195], v199 offset:17408
	s_waitcnt lgkmcnt(11)
	v_smfmac_f32_16x16x64_f16 v[230:233], v[138:141], a[80:87], v210
	v_mul_f32_e32 v253, 0x3dbaaaab, v172
	v_fmac_f32_e32 v253, 0x3ee6024d, v167
	v_smfmac_f32_16x16x64_f16 v[234:237], v[138:141], v[222:229], v210
	ds_read_b128 v[222:225], v199 offset:20480
	ds_read_b128 v[226:229], v199 offset:21504
	s_waitcnt lgkmcnt(12)
	v_smfmac_f32_16x16x64_f16 v[230:233], v[142:145], a[112:119], v210
	v_fmac_f32_e32 v253, 0x3f26aaab, v196
	v_fmac_f32_e32 v253, 0xbea50e7e, v220
	s_waitcnt lgkmcnt(4)
	v_smfmac_f32_16x16x64_f16 v[234:237], v[142:145], v[180:187], v210
	ds_read_b128 v[180:183], v199 offset:24576
	ds_read_b128 v[184:187], v199 offset:25600
	v_smfmac_f32_16x16x64_f16 v[230:233], v[146:149], a[144:151], v210
	v_mul_f32_e32 v254, 0x3dbaaaab, v175
	v_fmac_f32_e32 v254, 0x3ee6024d, v176
	s_waitcnt lgkmcnt(4)
	v_smfmac_f32_16x16x64_f16 v[234:237], v[146:149], v[188:195], v210
	ds_read_b128 v[188:191], v199 offset:28672
	ds_read_b128 v[192:195], v199 offset:29696
	v_smfmac_f32_16x16x64_f16 v[230:233], v[150:153], a[176:183], v210
	v_fmac_f32_e32 v254, 0x3f26aaab, v197
	v_fmac_f32_e32 v254, 0xbea50e7e, v246
	s_waitcnt lgkmcnt(4)
	v_smfmac_f32_16x16x64_f16 v[234:237], v[150:153], v[222:229], v210
	ds_read_b128 v[222:225], v199 offset:2048
	ds_read_b128 v[226:229], v199 offset:3072
	v_smfmac_f32_16x16x64_f16 v[230:233], v[154:157], a[208:215], v210
	v_mul_f32_e32 v255, 0x3dbaaaab, v174
	v_fmac_f32_e32 v255, 0x3ee6024d, v177
	s_waitcnt lgkmcnt(4)
	v_smfmac_f32_16x16x64_f16 v[234:237], v[154:157], v[180:187], v210
	ds_read_b128 v[180:183], v199 offset:6144
	ds_read_b128 v[184:187], v199 offset:7168
	v_smfmac_f32_16x16x64_f16 v[230:233], v[158:161], a[240:247], v210
	v_fmac_f32_e32 v255, 0x3f26aaab, v198
	v_fmac_f32_e32 v255, 0xbea50e7e, v247
	s_waitcnt lgkmcnt(4)
	v_smfmac_f32_16x16x64_f16 v[234:237], v[158:161], v[188:195], v210
	ds_read_b128 v[188:191], v199 offset:10240
	ds_read_b128 v[192:195], v199 offset:11264
	v_smfmac_f32_16x16x64_f16 v[238:241], v[130:133], a[24:31], v210
	s_waitcnt lgkmcnt(4)
	v_smfmac_f32_16x16x64_f16 v[242:245], v[130:133], v[222:229], v210
	ds_read_b128 v[222:225], v199 offset:14336
	ds_read_b128 v[226:229], v199 offset:15360
	v_smfmac_f32_16x16x64_f16 v[238:241], v[134:137], a[56:63], v210
	v_fmac_f32_e32 v230, s40, v231
	v_fmac_f32_e32 v234, s40, v235
	v_fmac_f32_e32 v230, s41, v232
	s_waitcnt lgkmcnt(4)
	v_smfmac_f32_16x16x64_f16 v[242:245], v[134:137], v[180:187], v210
	ds_read_b128 v[180:183], v199 offset:18432
	ds_read_b128 v[184:187], v199 offset:19456
	v_smfmac_f32_16x16x64_f16 v[238:241], v[138:141], a[88:95], v210
	v_fmac_f32_e32 v234, s41, v236
	s_nop 1
	v_permlane32_swap_b32_e32 v230, v234
	v_add_f32_e32 v250, v230, v234
	s_waitcnt lgkmcnt(4)
	v_smfmac_f32_16x16x64_f16 v[242:245], v[138:141], v[188:195], v210
	ds_read_b128 v[188:191], v199 offset:22528
	ds_read_b128 v[192:195], v199 offset:23552
	v_smfmac_f32_16x16x64_f16 v[238:241], v[142:145], a[120:127], v210
	v_fmac_f32_e32 v254, 0x3e061862, v250
	v_mov_b32_e32 v236, v254
	v_fma_mixlo_f16 v232, v178, v236, v169
	s_waitcnt lgkmcnt(4)
	v_smfmac_f32_16x16x64_f16 v[242:245], v[142:145], v[222:229], v210
	ds_read_b128 v[222:225], v199 offset:26624
	ds_read_b128 v[226:229], v199 offset:27648
	v_smfmac_f32_16x16x64_f16 v[238:241], v[146:149], a[152:159], v210
	v_fma_f32 v254, v178, v236, v169
	v_fma_mix_f32 v231, v254, 1.0, -v232 op_sel_hi:[0,0,1]
	v_fma_mixlo_f16 v235, v231, s42, 0
	s_waitcnt lgkmcnt(4)
	v_smfmac_f32_16x16x64_f16 v[242:245], v[146:149], v[180:187], v210
	ds_read_b128 v[180:183], v199 offset:30720
	ds_read_b128 v[184:187], v199 offset:31744
	v_smfmac_f32_16x16x64_f16 v[238:241], v[150:153], a[184:191], v210
	v_fma_mix_f32 v231, v231, s42, -v235 op_sel_hi:[0,0,1]
	v_fma_mixlo_f16 v233, v231, s42, 0
	ds_write_b16 v206, v232 offset:8704
	s_waitcnt lgkmcnt(5)
	v_smfmac_f32_16x16x64_f16 v[242:245], v[150:153], v[188:195], v210
	v_smfmac_f32_16x16x64_f16 v[238:241], v[154:157], a[216:223], v210
	ds_write_b16 v206, v235 offset:9248
	ds_write_b16 v206, v233 offset:9792
	s_waitcnt lgkmcnt(5)
	v_smfmac_f32_16x16x64_f16 v[242:245], v[154:157], v[222:229], v210
	v_smfmac_f32_16x16x64_f16 v[238:241], v[158:161], a[248:255], v210
	ds_read_b128 v[230:233], v217
	ds_read_b128 v[234:237], v217
	s_waitcnt lgkmcnt(5)
	v_smfmac_f32_16x16x64_f16 v[242:245], v[158:161], v[180:187], v210
	s_waitcnt lgkmcnt(1)
	v_smfmac_f32_16x16x64_f16 v[230:233], v[130:133], a[0:7], v210
	s_waitcnt lgkmcnt(0)
	v_smfmac_f32_16x16x64_f16 v[234:237], v[130:133], v[18:25], v210
	v_smfmac_f32_16x16x64_f16 v[230:233], v[134:137], a[40:47], v210
	v_fmac_f32_e32 v238, s40, v239
	v_fmac_f32_e32 v242, s40, v243
	v_fmac_f32_e32 v238, s41, v240
	v_smfmac_f32_16x16x64_f16 v[234:237], v[134:137], v[34:41], v210
	v_smfmac_f32_16x16x64_f16 v[230:233], v[138:141], a[64:71], v210
	v_fmac_f32_e32 v242, s41, v244
	s_nop 1
	v_permlane32_swap_b32_e32 v238, v242
	v_add_f32_e32 v251, v238, v242
	v_smfmac_f32_16x16x64_f16 v[234:237], v[138:141], v[42:49], v210
	v_smfmac_f32_16x16x64_f16 v[230:233], v[142:145], a[96:103], v210
	v_fmac_f32_e32 v255, 0x3e061862, v251
	v_mov_b32_e32 v244, v255
	v_fma_mixlo_f16 v240, v178, v244, v168
	v_smfmac_f32_16x16x64_f16 v[234:237], v[142:145], v[58:65], v210
	v_smfmac_f32_16x16x64_f16 v[230:233], v[146:149], a[128:135], v210
	v_fma_f32 v255, v178, v244, v168
	v_fma_mix_f32 v239, v255, 1.0, -v240 op_sel_hi:[0,0,1]
	v_fma_mixlo_f16 v243, v239, s42, 0
	v_smfmac_f32_16x16x64_f16 v[234:237], v[146:149], v[74:81], v210
	v_smfmac_f32_16x16x64_f16 v[230:233], v[150:153], a[160:167], v210
	v_fma_mix_f32 v239, v239, s42, -v243 op_sel_hi:[0,0,1]
	v_fma_mixlo_f16 v241, v239, s42, 0
	ds_write_b16 v207, v240 offset:8704
	v_smfmac_f32_16x16x64_f16 v[234:237], v[150:153], v[98:105], v210
	v_smfmac_f32_16x16x64_f16 v[230:233], v[154:157], a[192:199], v210
	ds_write_b16 v207, v243 offset:9248
	ds_write_b16 v207, v241 offset:9792
	v_smfmac_f32_16x16x64_f16 v[234:237], v[154:157], v[106:113], v210
	v_smfmac_f32_16x16x64_f16 v[230:233], v[158:161], a[224:231], v210
	ds_read_b128 v[238:241], v217
	ds_read_b128 v[242:245], v217
	v_smfmac_f32_16x16x64_f16 v[234:237], v[158:161], v[122:129], v210
	s_waitcnt lgkmcnt(1)
	v_smfmac_f32_16x16x64_f16 v[238:241], v[130:133], a[8:15], v210
	s_waitcnt lgkmcnt(0)
	v_smfmac_f32_16x16x64_f16 v[242:245], v[130:133], v[2:9], v210
	v_smfmac_f32_16x16x64_f16 v[238:241], v[134:137], a[32:39], v210
	v_fmac_f32_e32 v230, s40, v231
	v_fmac_f32_e32 v234, s40, v235
	v_fmac_f32_e32 v230, s41, v232
	v_smfmac_f32_16x16x64_f16 v[242:245], v[134:137], v[10:17], v210
	v_smfmac_f32_16x16x64_f16 v[238:241], v[138:141], a[72:79], v210
	v_fmac_f32_e32 v234, s41, v236
	s_nop 1
	v_permlane32_swap_b32_e32 v230, v234
	v_add_f32_e32 v248, v230, v234
	v_smfmac_f32_16x16x64_f16 v[242:245], v[138:141], v[50:57], v210
	v_smfmac_f32_16x16x64_f16 v[238:241], v[142:145], a[104:111], v210
	v_fmac_f32_e32 v252, 0x3e061862, v248
	v_mov_b32_e32 v236, v252
	v_fma_mixlo_f16 v232, v178, v236, v171
	v_smfmac_f32_16x16x64_f16 v[242:245], v[142:145], v[26:33], v210
	v_smfmac_f32_16x16x64_f16 v[238:241], v[146:149], a[136:143], v210
	v_fma_f32 v252, v178, v236, v171
	v_fma_mix_f32 v231, v252, 1.0, -v232 op_sel_hi:[0,0,1]
	v_fma_mixlo_f16 v235, v231, s42, 0
	v_smfmac_f32_16x16x64_f16 v[242:245], v[146:149], v[82:89], v210
	v_smfmac_f32_16x16x64_f16 v[238:241], v[150:153], a[168:175], v210
	v_fma_mix_f32 v231, v231, s42, -v235 op_sel_hi:[0,0,1]
	v_fma_mixlo_f16 v233, v231, s42, 0
	ds_write_b16 v204, v232 offset:8704
	v_smfmac_f32_16x16x64_f16 v[242:245], v[150:153], v[66:73], v210
	v_smfmac_f32_16x16x64_f16 v[238:241], v[154:157], a[200:207], v210
	ds_write_b16 v204, v235 offset:9248
	ds_write_b16 v204, v233 offset:9792
	v_smfmac_f32_16x16x64_f16 v[242:245], v[154:157], v[114:121], v210
	v_smfmac_f32_16x16x64_f16 v[238:241], v[158:161], a[232:239], v210
	ds_read_b128 v[230:233], v217
	ds_read_b128 v[234:237], v217
	v_smfmac_f32_16x16x64_f16 v[242:245], v[158:161], v[90:97], v210
	s_nop 4
	v_fmac_f32_e32 v238, s40, v239
	s_nop 1
	v_fmac_f32_e32 v242, s40, v243
	v_fmac_f32_e32 v238, s41, v240
	v_fmac_f32_e32 v242, s41, v244
	s_nop 1
	v_permlane32_swap_b32_e32 v238, v242
	v_add_f32_e32 v249, v238, v242
	v_fmac_f32_e32 v253, 0x3e061862, v249
	v_mov_b32_e32 v244, v253
	v_fma_mixlo_f16 v240, v178, v244, v170
	v_fma_f32 v253, v178, v244, v170
	v_fma_mix_f32 v239, v253, 1.0, -v240 op_sel_hi:[0,0,1]
	v_fma_mixlo_f16 v243, v239, s42, 0
	v_fma_mix_f32 v239, v239, s42, -v243 op_sel_hi:[0,0,1]
	v_fma_mixlo_f16 v241, v239, s42, 0
	ds_write_b16 v205, v240 offset:8704
	ds_write_b16 v205, v243 offset:9248
	ds_write_b16 v205, v241 offset:9792
	ds_read_b128 v[180:183], v199 offset:0
	ds_read_b128 v[184:187], v199 offset:1024
	ds_read_b128 v[188:191], v199 offset:4096
	ds_read_b128 v[192:195], v199 offset:5120
	ds_read_b128 v[222:225], v199 offset:8192
	s_waitcnt lgkmcnt(6)
	ds_read_b128 v[226:229], v199 offset:9216
	s_waitcnt lgkmcnt(0)
	s_barrier
	ds_read_b128 v[130:133], v208 offset:8704
	ds_read_b128 v[134:137], v209 offset:8768
	ds_read_b128 v[138:141], v211 offset:8704
	ds_read_b128 v[142:145], v212 offset:8704
	ds_read_b128 v[146:149], v213 offset:8704
	ds_read_b128 v[150:153], v214 offset:8704
	ds_read_b128 v[154:157], v215 offset:8704
	ds_read_b128 v[158:161], v216 offset:8704
	s_waitcnt lgkmcnt(7)
	v_smfmac_f32_16x16x64_f16 v[230:233], v[130:133], a[16:23], v210
	ds_read_b128 v[238:241], v217
	ds_read_b128 v[242:245], v217
	v_mul_f32_e32 v162, 0x3aa1907f, v173
	v_fmac_f32_e32 v162, 0xbb8b5ad3, v166
	v_smfmac_f32_16x16x64_f16 v[234:237], v[130:133], v[180:187], v210
	ds_read_b128 v[180:183], v199 offset:12288
	ds_read_b128 v[184:187], v199 offset:13312
	s_waitcnt lgkmcnt(10)
	v_smfmac_f32_16x16x64_f16 v[230:233], v[134:137], a[48:55], v210
	v_fmac_f32_e32 v162, 0x3d177777, v179
	v_fmac_f32_e32 v162, 0xbd50568f, v219
	v_fmac_f32_e32 v162, 0x3d2ba454, v248
	v_mul_f32_e32 v163, 0x3aa1907f, v172
	v_smfmac_f32_16x16x64_f16 v[234:237], v[134:137], v[188:195], v210
	ds_read_b128 v[188:191], v199 offset:16384
	ds_read_b128 v[192:195], v199 offset:17408
	s_waitcnt lgkmcnt(11)
	v_smfmac_f32_16x16x64_f16 v[230:233], v[138:141], a[80:87], v210
	v_fmac_f32_e32 v163, 0xbb8b5ad3, v167
	v_fmac_f32_e32 v163, 0x3d177777, v196
	v_fmac_f32_e32 v163, 0xbd50568f, v220
	v_fmac_f32_e32 v163, 0x3d2ba454, v249
	v_smfmac_f32_16x16x64_f16 v[234:237], v[138:141], v[222:229], v210
	ds_read_b128 v[222:225], v199 offset:20480
	ds_read_b128 v[226:229], v199 offset:21504
	s_waitcnt lgkmcnt(12)
	v_smfmac_f32_16x16x64_f16 v[230:233], v[142:145], a[112:119], v210
	v_mul_f32_e32 v164, 0x3aa1907f, v175
	v_fmac_f32_e32 v164, 0xbb8b5ad3, v176
	v_fmac_f32_e32 v164, 0x3d177777, v197
	v_fmac_f32_e32 v164, 0xbd50568f, v246
	s_waitcnt lgkmcnt(4)
	v_smfmac_f32_16x16x64_f16 v[234:237], v[142:145], v[180:187], v210
	ds_read_b128 v[180:183], v199 offset:24576
	ds_read_b128 v[184:187], v199 offset:25600
	v_smfmac_f32_16x16x64_f16 v[230:233], v[146:149], a[144:151], v210
	v_fmac_f32_e32 v164, 0x3d2ba454, v250
	v_mul_f32_e32 v165, 0x3aa1907f, v174
	v_fmac_f32_e32 v165, 0xbb8b5ad3, v177
	v_fmac_f32_e32 v165, 0x3d177777, v198
	s_waitcnt lgkmcnt(4)
	v_smfmac_f32_16x16x64_f16 v[234:237], v[146:149], v[188:195], v210
	ds_read_b128 v[188:191], v199 offset:28672
	ds_read_b128 v[192:195], v199 offset:29696
	v_smfmac_f32_16x16x64_f16 v[230:233], v[150:153], a[176:183], v210
	v_fmac_f32_e32 v165, 0xbd50568f, v247
	v_fmac_f32_e32 v165, 0x3d2ba454, v251
	v_max_f32_e64 v179, |v171|, |v252|
	v_mov_b32_e32 v248, 0x358637bd
	s_waitcnt lgkmcnt(4)
	v_smfmac_f32_16x16x64_f16 v[234:237], v[150:153], v[222:229], v210
	ds_read_b128 v[222:225], v199 offset:2048
	ds_read_b128 v[226:229], v199 offset:3072
	v_smfmac_f32_16x16x64_f16 v[230:233], v[154:157], a[208:215], v210
	v_fmac_f32_e32 v248, 0x3a83126f, v179
	v_rcp_f32_e32 v179, v248
	v_max_f32_e64 v196, |v170|, |v253|
	v_mov_b32_e32 v249, 0x358637bd
	s_waitcnt lgkmcnt(4)
	v_smfmac_f32_16x16x64_f16 v[234:237], v[154:157], v[180:187], v210
	ds_read_b128 v[180:183], v199 offset:6144
	ds_read_b128 v[184:187], v199 offset:7168
	v_smfmac_f32_16x16x64_f16 v[230:233], v[158:161], a[240:247], v210
	v_fmac_f32_e32 v249, 0x3a83126f, v196
	v_rcp_f32_e32 v196, v249
	v_max_f32_e64 v197, |v169|, |v254|
	v_mov_b32_e32 v250, 0x358637bd
	s_waitcnt lgkmcnt(4)
	v_smfmac_f32_16x16x64_f16 v[234:237], v[158:161], v[188:195], v210
	ds_read_b128 v[188:191], v199 offset:10240
	ds_read_b128 v[192:195], v199 offset:11264
	v_fmac_f32_e32 v250, 0x3a83126f, v197
	v_rcp_f32_e32 v197, v250
	v_max_f32_e64 v198, |v168|, |v255|
	v_mov_b32_e32 v251, 0x358637bd
	v_fmac_f32_e32 v251, 0x3a83126f, v198
	v_rcp_f32_e32 v198, v251
	v_smfmac_f32_16x16x64_f16 v[238:241], v[130:133], a[24:31], v210
	s_waitcnt lgkmcnt(4)
	v_smfmac_f32_16x16x64_f16 v[242:245], v[130:133], v[222:229], v210
	ds_read_b128 v[222:225], v199 offset:14336
	ds_read_b128 v[226:229], v199 offset:15360
	v_smfmac_f32_16x16x64_f16 v[238:241], v[134:137], a[56:63], v210
	v_fmac_f32_e32 v230, s40, v231
	v_fmac_f32_e32 v234, s40, v235
	s_waitcnt lgkmcnt(4)
	v_smfmac_f32_16x16x64_f16 v[242:245], v[134:137], v[180:187], v210
	ds_read_b128 v[180:183], v199 offset:18432
	ds_read_b128 v[184:187], v199 offset:19456
	v_smfmac_f32_16x16x64_f16 v[238:241], v[138:141], a[88:95], v210
	v_fmac_f32_e32 v230, s41, v232
	v_fmac_f32_e32 v234, s41, v236
	s_waitcnt lgkmcnt(4)
	v_smfmac_f32_16x16x64_f16 v[242:245], v[138:141], v[188:195], v210
	ds_read_b128 v[188:191], v199 offset:22528
	ds_read_b128 v[192:195], v199 offset:23552
	v_smfmac_f32_16x16x64_f16 v[238:241], v[142:145], a[120:127], v210
	v_permlane32_swap_b32_e32 v230, v234
	v_add_f32_e32 v176, v230, v234
	s_waitcnt lgkmcnt(4)
	v_smfmac_f32_16x16x64_f16 v[242:245], v[142:145], v[222:229], v210
	ds_read_b128 v[222:225], v199 offset:26624
	ds_read_b128 v[226:229], v199 offset:27648
	v_smfmac_f32_16x16x64_f16 v[238:241], v[146:149], a[152:159], v210
	v_fmac_f32_e32 v164, 0xbccccccd, v176
	v_mul_f32_e32 v231, v178, v164
	s_waitcnt lgkmcnt(4)
	v_smfmac_f32_16x16x64_f16 v[242:245], v[146:149], v[180:187], v210
	ds_read_b128 v[180:183], v199 offset:30720
	ds_read_b128 v[184:187], v199 offset:31744
	v_smfmac_f32_16x16x64_f16 v[238:241], v[150:153], a[184:191], v210
	v_mul_f32_e32 v231, v231, v197
	v_mul_f32_e32 v219, v231, v231
	s_waitcnt lgkmcnt(4)
	v_smfmac_f32_16x16x64_f16 v[242:245], v[150:153], v[188:195], v210
	v_smfmac_f32_16x16x64_f16 v[238:241], v[154:157], a[216:223], v210
	ds_read_b128 v[230:233], v217
	ds_read_b128 v[234:237], v217
	s_waitcnt lgkmcnt(4)
	v_smfmac_f32_16x16x64_f16 v[242:245], v[154:157], v[222:229], v210
	v_smfmac_f32_16x16x64_f16 v[238:241], v[158:161], a[248:255], v210
	s_waitcnt lgkmcnt(2)
	v_smfmac_f32_16x16x64_f16 v[242:245], v[158:161], v[180:187], v210
	s_waitcnt lgkmcnt(1)
	v_smfmac_f32_16x16x64_f16 v[230:233], v[130:133], a[0:7], v210
	s_waitcnt lgkmcnt(0)
	v_smfmac_f32_16x16x64_f16 v[234:237], v[130:133], v[18:25], v210
	v_smfmac_f32_16x16x64_f16 v[230:233], v[134:137], a[40:47], v210
	v_fmac_f32_e32 v238, s40, v239
	v_fmac_f32_e32 v242, s40, v243
	v_smfmac_f32_16x16x64_f16 v[234:237], v[134:137], v[34:41], v210
	v_smfmac_f32_16x16x64_f16 v[230:233], v[138:141], a[64:71], v210
	v_fmac_f32_e32 v238, s41, v240
	v_fmac_f32_e32 v242, s41, v244
	v_smfmac_f32_16x16x64_f16 v[234:237], v[138:141], v[42:49], v210
	v_smfmac_f32_16x16x64_f16 v[230:233], v[142:145], a[96:103], v210
	v_permlane32_swap_b32_e32 v238, v242
	v_add_f32_e32 v177, v238, v242
	v_smfmac_f32_16x16x64_f16 v[234:237], v[142:145], v[58:65], v210
	v_smfmac_f32_16x16x64_f16 v[230:233], v[146:149], a[128:135], v210
	v_fmac_f32_e32 v165, 0xbccccccd, v177
	v_mul_f32_e32 v239, v178, v165
	v_smfmac_f32_16x16x64_f16 v[234:237], v[146:149], v[74:81], v210
	v_smfmac_f32_16x16x64_f16 v[230:233], v[150:153], a[160:167], v210
	v_mul_f32_e32 v239, v239, v198
	v_fmac_f32_e32 v219, v239, v239
	v_smfmac_f32_16x16x64_f16 v[234:237], v[150:153], v[98:105], v210
	v_smfmac_f32_16x16x64_f16 v[230:233], v[154:157], a[192:199], v210
	ds_read_b128 v[238:241], v217
	ds_read_b128 v[242:245], v217
	v_smfmac_f32_16x16x64_f16 v[234:237], v[154:157], v[106:113], v210
	v_smfmac_f32_16x16x64_f16 v[230:233], v[158:161], a[224:231], v210
	v_smfmac_f32_16x16x64_f16 v[234:237], v[158:161], v[122:129], v210
	s_waitcnt lgkmcnt(1)
	v_smfmac_f32_16x16x64_f16 v[238:241], v[130:133], a[8:15], v210
	s_waitcnt lgkmcnt(0)
	v_smfmac_f32_16x16x64_f16 v[242:245], v[130:133], v[2:9], v210
	v_smfmac_f32_16x16x64_f16 v[238:241], v[134:137], a[32:39], v210
	v_fmac_f32_e32 v230, s40, v231
	v_fmac_f32_e32 v234, s40, v235
	v_smfmac_f32_16x16x64_f16 v[242:245], v[134:137], v[10:17], v210
	v_smfmac_f32_16x16x64_f16 v[238:241], v[138:141], a[72:79], v210
	v_fmac_f32_e32 v230, s41, v232
	v_fmac_f32_e32 v234, s41, v236
	v_smfmac_f32_16x16x64_f16 v[242:245], v[138:141], v[50:57], v210
	v_smfmac_f32_16x16x64_f16 v[238:241], v[142:145], a[104:111], v210
	v_permlane32_swap_b32_e32 v230, v234
	v_add_f32_e32 v166, v230, v234
	v_smfmac_f32_16x16x64_f16 v[242:245], v[142:145], v[26:33], v210
	v_smfmac_f32_16x16x64_f16 v[238:241], v[146:149], a[136:143], v210
	v_fmac_f32_e32 v162, 0xbccccccd, v166
	v_mul_f32_e32 v231, v178, v162
	v_smfmac_f32_16x16x64_f16 v[242:245], v[146:149], v[82:89], v210
	v_smfmac_f32_16x16x64_f16 v[238:241], v[150:153], a[168:175], v210
	v_mul_f32_e32 v231, v231, v179
	v_fmac_f32_e32 v219, v231, v231
	v_smfmac_f32_16x16x64_f16 v[242:245], v[150:153], v[66:73], v210
	v_smfmac_f32_16x16x64_f16 v[238:241], v[154:157], a[200:207], v210
	ds_read_b128 v[230:233], v217
	ds_read_b128 v[234:237], v217
	v_smfmac_f32_16x16x64_f16 v[242:245], v[154:157], v[114:121], v210
	v_smfmac_f32_16x16x64_f16 v[238:241], v[158:161], a[232:239], v210
	v_smfmac_f32_16x16x64_f16 v[242:245], v[158:161], v[90:97], v210
	s_nop 6
	v_fmac_f32_e32 v238, s40, v239
	v_fmac_f32_e32 v242, s40, v243
	v_fmac_f32_e32 v238, s41, v240
	v_fmac_f32_e32 v242, s41, v244
	s_nop 1
	v_permlane32_swap_b32_e32 v238, v242
	v_add_f32_e32 v167, v238, v242
	v_fmac_f32_e32 v163, 0xbccccccd, v167
	v_mul_f32_e32 v239, v178, v163
	v_mul_f32_e32 v239, v239, v196
	v_fmac_f32_e32 v219, v239, v239
	ds_read_b128 v[180:183], v199 offset:0
	ds_read_b128 v[184:187], v199 offset:1024
	ds_read_b128 v[188:191], v199 offset:4096
	ds_read_b128 v[192:195], v199 offset:5120
	ds_read_b128 v[222:225], v199 offset:8192
	ds_read_b128 v[226:229], v199 offset:9216
	v_add_f32_dpp v238, v219, v219 quad_perm:[1,0,3,2] row_mask:0xf bank_mask:0xf bound_ctrl:1
	s_nop 1
	v_add_f32_dpp v238, v238, v238 quad_perm:[2,3,0,1] row_mask:0xf bank_mask:0xf bound_ctrl:1
	s_nop 1
	v_add_f32_dpp v238, v238, v238 row_half_mirror row_mask:0xf bank_mask:0xf bound_ctrl:1
	s_nop 1
	v_add_f32_dpp v238, v238, v238 row_mirror row_mask:0xf bank_mask:0xf bound_ctrl:1
	v_mov_b32_e32 v239, v238
	s_nop 1
	v_permlane32_swap_b32_e32 v238, v239
	v_add_f32_e32 v238, v238, v239
	v_lshl_add_u32 v240, s29, 6, v218
	v_lshlrev_b32_e32 v241, 3, v201
	v_or_b32_e32 v241, 0x24400, v241
	v_lshl_add_u32 v241, s29, 6, v241
	s_and_saveexec_b64 s[2:3], s[4:5]
	ds_write_b32 v240, v238
	s_or_b64 exec, exec, s[2:3]
	s_waitcnt lgkmcnt(0)
	s_barrier
	ds_read2_b32 v[130:131], v241 offset1:4
	ds_read2_b32 v[132:133], v241 offset0:8 offset1:12
	s_waitcnt lgkmcnt(1)
	v_add_f32_e32 v238, v130, v131
	s_waitcnt lgkmcnt(0)
	v_add_f32_e32 v238, v238, v132
	v_add_f32_e32 v238, v238, v133
	v_mul_f32_e32 v238, 0x3b000000, v238
	v_max_f32_e32 v238, 0xda24260, v238
	v_sqrt_f32_e32 v238, v238
	s_nop 0
	v_cmp_ngt_f32_e64 s[2:3], 1.0, v238
	v_cmp_gt_f32_e32 vcc, 1.0, v238
	v_log_f32_e32 v239, v238
	v_mul_f32_e32 v241, 0x44000000, v178
	s_and_saveexec_b64 s[26:27], vcc
	v_add_f32_e32 v221, v221, v241
	v_mov_b32_e32 v171, v252
	v_mov_b32_e32 v173, v166
	v_mov_b32_e32 v170, v253
	v_mov_b32_e32 v172, v167
	v_mov_b32_e32 v169, v254
	v_mov_b32_e32 v175, v176
	v_mov_b32_e32 v168, v255
	v_mov_b32_e32 v174, v177
	s_or_b64 exec, exec, s[26:27]
	v_mov_b32_e32 v240, 0x41200000
	s_nop 0
	v_cndmask_b32_e64 v240, v240, 1.0, s[22:23]
	s_xor_b32 s29, s29, 1
	s_add_i32 s30, s30, 1
	v_mul_f32_e32 v239, 0xbe4ccccd, v239
	v_exp_f32_e32 v239, v239
	s_nop 0
	v_mul_f32_e32 v239, 0x3f666666, v239
	v_min_f32_e32 v240, v239, v240
	v_max_f32_e32 v239, 0x3e4ccccd, v239
	v_cndmask_b32_e64 v239, v240, v239, s[2:3]
	v_mul_f32_e32 v1, v241, v239
	s_mov_b64 s[22:23], s[2:3]
	s_branch .Lrk_top
